# P4 router: table LDS-DMA wait moved behind the first group's 32 row loads (vmcnt(32) + barrier before the table reads) so the two fetches overlap
# speedup vs baseline: 1.0028x; 1.0028x over previous
.LBB0_430:
	v_cmp_gt_i32_e64 s[4:5], 32, v161
	s_and_saveexec_b64 s[10:11], s[4:5]
	v_lshl_add_u32 v2, v161, 2, 0
	v_add_u32_e32 v2, 0x24600, v2
	v_mov_b32_e32 v3, 0
	ds_write_b32 v2, v3
	s_or_b64 exec, exec, s[10:11]
	s_cmpk_gt_i32 s82, 0xff
	s_waitcnt lgkmcnt(0)
	s_barrier
	s_cbranch_scc1 .LBB0_445
	v_and_b32_e32 v171, 15, v161
	v_lshlrev_b32_e32 v4, 2, v171
	global_load_dword v172, v4, s[6:7]
	global_load_dword v173, v4, s[6:7] offset:64
	s_add_i32 s0, 0, 0x10200
	s_add_u32 s14, s12, 0x100000
	v_mul_u32_u24_e32 v2, 0x810, v171
	v_and_b32_e32 v3, 48, v161
	s_addc_u32 s15, s13, 0
	v_mov_b32_e32 v139, 0
	v_add3_u32 v174, 0, v2, v3
	v_add3_u32 v175, s0, v2, v3
	s_add_u32 s16, s12, 0x900000
	v_lshrrev_b32_e32 v5, 4, v170
	v_and_b32_e32 v2, 48, v170
	v_mov_b32_e32 v3, v139
	s_addc_u32 s17, s13, 0
	v_lshlrev_b32_e32 v138, 3, v5
	v_lshl_add_u64 v[2:3], s[12:13], 0, v[2:3]
	s_mov_b64 s[2:3], 0x36c00000
	s_add_u32 s18, s12, 0x1100000
	v_lshl_add_u64 v[140:141], v[2:3], 0, s[2:3]
	v_lshl_add_u64 v[2:3], s[12:13], 0, v[138:139]
	s_mov_b64 s[2:3], 0xdc00000
	s_addc_u32 s19, s13, 0
	s_mul_i32 s0, s8, 0x840
	v_lshl_add_u64 v[142:143], v[2:3], 0, s[2:3]
	v_lshlrev_b32_e32 v2, 2, v5
	v_lshlrev_b32_e32 v3, 2, v161
	s_add_i32 s1, 0, 0x24600
	s_add_i32 s2, 0, 0x24680
	s_add_i32 s0, s0, 0
	v_add_u32_e32 v177, s1, v3
	v_add_u32_e32 v178, s2, v3
	v_or_b32_e32 v3, v2, v194
	s_add_i32 s0, s0, 0x20400
	v_lshlrev_b32_e32 v179, 2, v3
	v_mul_u32_u24_e32 v3, 0x210, v5
	v_or_b32_e32 v2, 1, v2
	s_lshl_b32 s9, s8, 5
	v_add3_u32 v180, s0, v3, v4
	v_or_b32_e32 v3, v2, v194
	v_mul_u32_u24_e32 v2, 0x84, v2
	s_lshl_b32 s3, s82, 8
	v_add3_u32 v182, s0, v2, v4
	s_add_i32 s3, s3, s9
	s_lshl_b32 s9, s82, 10
	s_lshl_b32 s8, s8, 7
	v_cmp_gt_u32_e64 s[6:7], 16, v170
	v_mul_u32_u24_e32 v176, 0x84, v170
	v_lshlrev_b32_e32 v181, 2, v3
	v_or_b32_e32 v183, 8, v179
	v_add_u32_e32 v184, 0x84, v182
	v_or_b32_e32 v185, 12, v179
	v_add_u32_e32 v186, 0x108, v182
	s_lshl_b32 s22, s88, 8
	v_lshlrev_b32_e32 v187, 2, v170
	s_add_i32 s23, s9, s8
	s_lshl_b32 s24, s88, 10
	v_mov_b32_e32 v195, 0x3727c5ac
	s_mov_b32 s25, 0xf800000
	v_mov_b32_e32 v196, 0x260
	v_mov_b32_e32 v197, 1
	s_movk_i32 s26, 0x80
	s_movk_i32 s27, 0x100
	s_movk_i32 s28, 0x200
	s_movk_i32 s29, 0x400
	s_movk_i32 s30, 0x800
	s_movk_i32 s31, 0x1000
	s_movk_i32 s33, 0x2000
	s_movk_i32 s34, 0x4000
	s_mov_b32 s35, 0x8000
	s_mov_b32 s36, 0x10000
	s_mov_b32 s37, 0x20000
	s_mov_b32 s38, 0x40000
	s_mov_b32 s39, 0x80000
	s_mov_b32 s40, 0x100000
	s_mov_b32 s41, 0x200000
	s_mov_b32 s42, 0x400000
	s_mov_b32 s43, 0x800000
	s_mov_b32 s44, 0x1000000
	s_brev_b32 s45, 64
	s_brev_b32 s46, 32
	s_brev_b32 s47, 16
	s_brev_b32 s48, 8
	s_brev_b32 s49, 4
	s_mov_b32 s50, 0x3fb8aa3b
	s_mov_b32 s51, 0xc2ce8ed0
	s_mov_b32 s52, 0x42b17218
	v_mov_b32_e32 v198, 0xff800000
	v_mov_b32_e32 v199, 0x7f800000
	s_mov_b32 s53, s82
	s_branch .LBB0_435

.LBB0_435:
	v_add_u32_e32 v166, s3, v171
	v_ashrrev_i32_e32 v167, 31, v166
	v_lshlrev_b64 v[2:3], 11, v[166:167]
	v_lshl_add_u64 v[2:3], v[140:141], 0, v[2:3]
	global_load_dwordx4 v[126:129], v[2:3], off
	global_load_dwordx4 v[122:125], v[2:3], off offset:64
	global_load_dwordx4 v[118:121], v[2:3], off offset:128
	global_load_dwordx4 v[114:117], v[2:3], off offset:192
	global_load_dwordx4 v[110:113], v[2:3], off offset:256
	global_load_dwordx4 v[106:109], v[2:3], off offset:320
	global_load_dwordx4 v[102:105], v[2:3], off offset:384
	global_load_dwordx4 v[98:101], v[2:3], off offset:448
	global_load_dwordx4 v[94:97], v[2:3], off offset:512
	global_load_dwordx4 v[90:93], v[2:3], off offset:576
	global_load_dwordx4 v[86:89], v[2:3], off offset:640
	global_load_dwordx4 v[82:85], v[2:3], off offset:704
	global_load_dwordx4 v[78:81], v[2:3], off offset:768
	global_load_dwordx4 v[74:77], v[2:3], off offset:832
	global_load_dwordx4 v[70:73], v[2:3], off offset:896
	global_load_dwordx4 v[66:69], v[2:3], off offset:960
	global_load_dwordx4 v[62:65], v[2:3], off offset:1024
	global_load_dwordx4 v[58:61], v[2:3], off offset:1088
	global_load_dwordx4 v[54:57], v[2:3], off offset:1152
	global_load_dwordx4 v[50:53], v[2:3], off offset:1216
	global_load_dwordx4 v[46:49], v[2:3], off offset:1280
	global_load_dwordx4 v[42:45], v[2:3], off offset:1344
	global_load_dwordx4 v[38:41], v[2:3], off offset:1408
	global_load_dwordx4 v[34:37], v[2:3], off offset:1472
	global_load_dwordx4 v[30:33], v[2:3], off offset:1536
	global_load_dwordx4 v[26:29], v[2:3], off offset:1600
	global_load_dwordx4 v[22:25], v[2:3], off offset:1664
	global_load_dwordx4 v[18:21], v[2:3], off offset:1728
	global_load_dwordx4 v[14:17], v[2:3], off offset:1792
	global_load_dwordx4 v[10:13], v[2:3], off offset:1856
	global_load_dwordx4 v[6:9], v[2:3], off offset:1920
	s_nop 0
	global_load_dwordx4 v[2:5], v[2:3], off offset:1984
	s_waitcnt vmcnt(32)
	s_barrier
	ds_read_b128 v[130:133], v175 offset:33024
	ds_read_b128 v[134:137], v175 offset:33088
	ds_read_b128 v[210:213], v175
	ds_read_b128 v[214:217], v175 offset:64
	ds_read_b128 v[218:221], v174 offset:33024
	ds_read_b128 v[222:225], v174 offset:33088
	ds_read_b128 v[226:229], v174
	ds_read_b128 v[230:233], v174 offset:64
	v_lshlrev_b64 v[168:169], 10, v[166:167]
	s_waitcnt vmcnt(31) lgkmcnt(1)
	v_mfma_f32_16x16x32_bf16 v[226:229], v[126:129], v[226:229], 0
	v_and_b32_e32 v147, 0xffff0000, v126
	v_and_b32_e32 v151, 0xffff0000, v127
	v_lshlrev_b32_e32 v145, 16, v126
	v_mfma_f32_16x16x32_bf16 v[218:221], v[126:129], v[218:221], 0
	v_lshlrev_b32_e32 v149, 16, v127
	v_and_b32_e32 v155, 0xffff0000, v128
	v_mul_f32_e32 v147, v147, v147
	v_mul_f32_e32 v151, v151, v151
	v_mfma_f32_16x16x32_bf16 v[210:213], v[126:129], v[210:213], v[226:229]
	v_lshlrev_b32_e32 v153, 16, v128
	v_and_b32_e32 v159, 0xffff0000, v129
	v_mul_f32_e32 v155, v155, v155
	v_mfma_f32_16x16x32_bf16 v[130:133], v[126:129], v[130:133], v[218:221]
	v_fmac_f32_e32 v147, v145, v145
	v_fmac_f32_e32 v151, v149, v149
	v_lshlrev_b32_e32 v157, 16, v129
	s_waitcnt vmcnt(30)
	v_and_b32_e32 v234, 0xffff0000, v122
	v_mul_f32_e32 v159, v159, v159
	v_fmac_f32_e32 v155, v153, v153
	v_add_f32_e32 v145, v147, v151
	v_lshlrev_b32_e32 v167, 16, v122
	v_and_b32_e32 v236, 0xffff0000, v123
	v_mul_f32_e32 v234, v234, v234
	v_fmac_f32_e32 v159, v157, v157
	v_add_f32_e32 v145, v155, v145
	v_lshlrev_b32_e32 v235, 16, v123
	v_and_b32_e32 v238, 0xffff0000, v124
	v_mul_f32_e32 v236, v236, v236
	v_fmac_f32_e32 v234, v167, v167
	s_waitcnt lgkmcnt(0)
	v_mfma_f32_16x16x32_bf16 v[210:213], v[122:125], v[230:233], v[210:213]
	v_add_f32_e32 v145, v159, v145
	v_lshlrev_b32_e32 v237, 16, v124
	v_and_b32_e32 v240, 0xffff0000, v125
	v_mfma_f32_16x16x32_bf16 v[130:133], v[122:125], v[222:225], v[130:133]
	v_mul_f32_e32 v238, v238, v238
	v_fmac_f32_e32 v236, v235, v235
	v_add_f32_e32 v145, v234, v145
	v_lshlrev_b32_e32 v239, 16, v125
	v_mul_f32_e32 v240, v240, v240
	v_fmac_f32_e32 v238, v237, v237
	v_add_f32_e32 v145, v236, v145
	v_fmac_f32_e32 v240, v239, v239
	v_add_f32_e32 v145, v238, v145
	v_mfma_f32_16x16x32_bf16 v[210:213], v[122:125], v[214:217], v[210:213]
	v_add_f32_e32 v145, v240, v145
	v_mfma_f32_16x16x32_bf16 v[130:133], v[122:125], v[134:137], v[130:133]
	s_waitcnt vmcnt(29)
	v_and_b32_e32 v149, 0xffff0000, v118
	v_lshlrev_b32_e32 v147, 16, v118
	v_mul_f32_e32 v149, v149, v149
	v_fmac_f32_e32 v149, v147, v147
	v_add_f32_e32 v145, v149, v145
	v_and_b32_e32 v149, 0xffff0000, v119
	v_lshlrev_b32_e32 v147, 16, v119
	v_mul_f32_e32 v149, v149, v149
	v_fmac_f32_e32 v149, v147, v147
	v_add_f32_e32 v145, v149, v145
	v_and_b32_e32 v149, 0xffff0000, v120
	v_lshlrev_b32_e32 v147, 16, v120
	v_mul_f32_e32 v149, v149, v149
	v_fmac_f32_e32 v149, v147, v147
	v_add_f32_e32 v145, v149, v145
	v_and_b32_e32 v149, 0xffff0000, v121
	ds_read_b128 v[134:137], v174 offset:128
	ds_read_b128 v[214:217], v174 offset:33152
	ds_read_b128 v[218:221], v175 offset:128
	ds_read_b128 v[222:225], v175 offset:33152
	ds_read_b128 v[226:229], v174 offset:192
	v_lshlrev_b32_e32 v147, 16, v121
	v_mul_f32_e32 v149, v149, v149
	s_waitcnt lgkmcnt(4)
	v_mfma_f32_16x16x32_bf16 v[134:137], v[118:121], v[134:137], v[210:213]
	v_fmac_f32_e32 v149, v147, v147
	v_add_f32_e32 v145, v149, v145
	s_waitcnt vmcnt(28)
	v_and_b32_e32 v149, 0xffff0000, v114
	s_waitcnt lgkmcnt(3)
	v_mfma_f32_16x16x32_bf16 v[130:133], v[118:121], v[214:217], v[130:133]
	v_lshlrev_b32_e32 v147, 16, v114
	v_mul_f32_e32 v149, v149, v149
	v_fmac_f32_e32 v149, v147, v147
	s_waitcnt lgkmcnt(2)
	v_mfma_f32_16x16x32_bf16 v[134:137], v[118:121], v[218:221], v[134:137]
	ds_read_b128 v[218:221], v174 offset:33216
	ds_read_b128 v[214:217], v175 offset:33216
	v_add_f32_e32 v145, v149, v145
	v_and_b32_e32 v149, 0xffff0000, v115
	s_waitcnt lgkmcnt(3)
	v_mfma_f32_16x16x32_bf16 v[130:133], v[118:121], v[222:225], v[130:133]
	v_lshlrev_b32_e32 v147, 16, v115
	v_mul_f32_e32 v149, v149, v149
	v_fmac_f32_e32 v149, v147, v147
	v_add_f32_e32 v145, v149, v145
	v_and_b32_e32 v149, 0xffff0000, v116
	ds_read_b128 v[210:213], v175 offset:192
	v_lshlrev_b32_e32 v147, 16, v116
	v_mul_f32_e32 v149, v149, v149
	s_waitcnt lgkmcnt(3)
	v_mfma_f32_16x16x32_bf16 v[134:137], v[114:117], v[226:229], v[134:137]
	v_fmac_f32_e32 v149, v147, v147
	v_add_f32_e32 v145, v149, v145
	v_and_b32_e32 v149, 0xffff0000, v117
	s_waitcnt lgkmcnt(2)
	v_mfma_f32_16x16x32_bf16 v[130:133], v[114:117], v[218:221], v[130:133]
	v_lshlrev_b32_e32 v147, 16, v117
	v_mul_f32_e32 v149, v149, v149
	v_fmac_f32_e32 v149, v147, v147
	s_waitcnt lgkmcnt(0)
	v_mfma_f32_16x16x32_bf16 v[134:137], v[114:117], v[210:213], v[134:137]
	v_add_f32_e32 v145, v149, v145
	v_mfma_f32_16x16x32_bf16 v[130:133], v[114:117], v[214:217], v[130:133]
	s_waitcnt vmcnt(27)
	v_and_b32_e32 v149, 0xffff0000, v110
	v_lshlrev_b32_e32 v147, 16, v110
	v_mul_f32_e32 v149, v149, v149
	v_fmac_f32_e32 v149, v147, v147
	v_add_f32_e32 v145, v149, v145
	v_and_b32_e32 v149, 0xffff0000, v111
	v_lshlrev_b32_e32 v147, 16, v111
	v_mul_f32_e32 v149, v149, v149
	v_fmac_f32_e32 v149, v147, v147
	v_add_f32_e32 v145, v149, v145
	v_and_b32_e32 v149, 0xffff0000, v112
	v_lshlrev_b32_e32 v147, 16, v112
	v_mul_f32_e32 v149, v149, v149
	v_fmac_f32_e32 v149, v147, v147
	v_add_f32_e32 v145, v149, v145
	v_and_b32_e32 v149, 0xffff0000, v113
	ds_read_b128 v[210:213], v174 offset:256
	ds_read_b128 v[214:217], v174 offset:33280
	ds_read_b128 v[218:221], v175 offset:256
	ds_read_b128 v[222:225], v175 offset:33280
	ds_read_b128 v[226:229], v174 offset:320
	v_lshlrev_b32_e32 v147, 16, v113
	v_mul_f32_e32 v149, v149, v149
	s_waitcnt lgkmcnt(4)
	v_mfma_f32_16x16x32_bf16 v[134:137], v[110:113], v[210:213], v[134:137]
	v_fmac_f32_e32 v149, v147, v147
	v_add_f32_e32 v145, v149, v145
	s_waitcnt vmcnt(26)
	v_and_b32_e32 v149, 0xffff0000, v106
	s_waitcnt lgkmcnt(3)
	v_mfma_f32_16x16x32_bf16 v[130:133], v[110:113], v[214:217], v[130:133]
	v_lshlrev_b32_e32 v147, 16, v106
	v_mul_f32_e32 v149, v149, v149
	v_fmac_f32_e32 v149, v147, v147
	s_waitcnt lgkmcnt(2)
	v_mfma_f32_16x16x32_bf16 v[134:137], v[110:113], v[218:221], v[134:137]
	ds_read_b128 v[218:221], v174 offset:33344
	ds_read_b128 v[214:217], v175 offset:33344
	v_add_f32_e32 v145, v149, v145
	v_and_b32_e32 v149, 0xffff0000, v107
	s_waitcnt lgkmcnt(3)
	v_mfma_f32_16x16x32_bf16 v[130:133], v[110:113], v[222:225], v[130:133]
	v_lshlrev_b32_e32 v147, 16, v107
	v_mul_f32_e32 v149, v149, v149
	v_fmac_f32_e32 v149, v147, v147
	v_add_f32_e32 v145, v149, v145
	v_and_b32_e32 v149, 0xffff0000, v108
	ds_read_b128 v[210:213], v175 offset:320
	v_lshlrev_b32_e32 v147, 16, v108
	v_mul_f32_e32 v149, v149, v149
	s_waitcnt lgkmcnt(3)
	v_mfma_f32_16x16x32_bf16 v[134:137], v[106:109], v[226:229], v[134:137]
	v_fmac_f32_e32 v149, v147, v147
	v_add_f32_e32 v145, v149, v145
	v_and_b32_e32 v149, 0xffff0000, v109
	s_waitcnt lgkmcnt(2)
	v_mfma_f32_16x16x32_bf16 v[130:133], v[106:109], v[218:221], v[130:133]
	v_lshlrev_b32_e32 v147, 16, v109
	v_mul_f32_e32 v149, v149, v149
	v_fmac_f32_e32 v149, v147, v147
	s_waitcnt lgkmcnt(0)
	v_mfma_f32_16x16x32_bf16 v[134:137], v[106:109], v[210:213], v[134:137]
	v_add_f32_e32 v145, v149, v145
	v_mfma_f32_16x16x32_bf16 v[130:133], v[106:109], v[214:217], v[130:133]
	s_waitcnt vmcnt(25)
	v_and_b32_e32 v149, 0xffff0000, v102
	v_lshlrev_b32_e32 v147, 16, v102
	v_mul_f32_e32 v149, v149, v149
	v_fmac_f32_e32 v149, v147, v147
	v_add_f32_e32 v145, v149, v145
	v_and_b32_e32 v149, 0xffff0000, v103
	v_lshlrev_b32_e32 v147, 16, v103
	v_mul_f32_e32 v149, v149, v149
	v_fmac_f32_e32 v149, v147, v147
	v_add_f32_e32 v145, v149, v145
	v_and_b32_e32 v149, 0xffff0000, v104
	v_lshlrev_b32_e32 v147, 16, v104
	v_mul_f32_e32 v149, v149, v149
	v_fmac_f32_e32 v149, v147, v147
	v_add_f32_e32 v145, v149, v145
	v_and_b32_e32 v149, 0xffff0000, v105
	ds_read_b128 v[210:213], v174 offset:384
	ds_read_b128 v[214:217], v174 offset:33408
	ds_read_b128 v[218:221], v175 offset:384
	ds_read_b128 v[222:225], v175 offset:33408
	ds_read_b128 v[226:229], v174 offset:448
	v_lshlrev_b32_e32 v147, 16, v105
	v_mul_f32_e32 v149, v149, v149
	s_waitcnt lgkmcnt(4)
	v_mfma_f32_16x16x32_bf16 v[134:137], v[102:105], v[210:213], v[134:137]
	v_fmac_f32_e32 v149, v147, v147
	v_add_f32_e32 v145, v149, v145
	s_waitcnt vmcnt(24)
	v_and_b32_e32 v149, 0xffff0000, v98
	s_waitcnt lgkmcnt(3)
	v_mfma_f32_16x16x32_bf16 v[130:133], v[102:105], v[214:217], v[130:133]
	v_lshlrev_b32_e32 v147, 16, v98
	v_mul_f32_e32 v149, v149, v149
	v_fmac_f32_e32 v149, v147, v147
	s_waitcnt lgkmcnt(2)
	v_mfma_f32_16x16x32_bf16 v[134:137], v[102:105], v[218:221], v[134:137]
	ds_read_b128 v[218:221], v174 offset:33472
	ds_read_b128 v[214:217], v175 offset:33472
	v_add_f32_e32 v145, v149, v145
	v_and_b32_e32 v149, 0xffff0000, v99
	s_waitcnt lgkmcnt(3)
	v_mfma_f32_16x16x32_bf16 v[130:133], v[102:105], v[222:225], v[130:133]
	v_lshlrev_b32_e32 v147, 16, v99
	v_mul_f32_e32 v149, v149, v149
	v_fmac_f32_e32 v149, v147, v147
	v_add_f32_e32 v145, v149, v145
	v_and_b32_e32 v149, 0xffff0000, v100
	ds_read_b128 v[210:213], v175 offset:448
	v_lshlrev_b32_e32 v147, 16, v100
	v_mul_f32_e32 v149, v149, v149
	s_waitcnt lgkmcnt(3)
	v_mfma_f32_16x16x32_bf16 v[134:137], v[98:101], v[226:229], v[134:137]
	v_fmac_f32_e32 v149, v147, v147
	v_add_f32_e32 v145, v149, v145
	v_and_b32_e32 v149, 0xffff0000, v101
	s_waitcnt lgkmcnt(2)
	v_mfma_f32_16x16x32_bf16 v[130:133], v[98:101], v[218:221], v[130:133]
	v_lshlrev_b32_e32 v147, 16, v101
	v_mul_f32_e32 v149, v149, v149
	v_fmac_f32_e32 v149, v147, v147
	s_waitcnt lgkmcnt(0)
	v_mfma_f32_16x16x32_bf16 v[134:137], v[98:101], v[210:213], v[134:137]
	v_add_f32_e32 v145, v149, v145
	v_mfma_f32_16x16x32_bf16 v[130:133], v[98:101], v[214:217], v[130:133]
	s_waitcnt vmcnt(23)
	v_and_b32_e32 v149, 0xffff0000, v94
	v_lshlrev_b32_e32 v147, 16, v94
	v_mul_f32_e32 v149, v149, v149
	v_fmac_f32_e32 v149, v147, v147
	v_add_f32_e32 v145, v149, v145
	v_and_b32_e32 v149, 0xffff0000, v95
	v_lshlrev_b32_e32 v147, 16, v95
	v_mul_f32_e32 v149, v149, v149
	v_fmac_f32_e32 v149, v147, v147
	v_add_f32_e32 v145, v149, v145
	v_and_b32_e32 v149, 0xffff0000, v96
	v_lshlrev_b32_e32 v147, 16, v96
	v_mul_f32_e32 v149, v149, v149
	v_fmac_f32_e32 v149, v147, v147
	v_add_f32_e32 v145, v149, v145
	v_and_b32_e32 v149, 0xffff0000, v97
	ds_read_b128 v[210:213], v174 offset:512
	ds_read_b128 v[214:217], v174 offset:33536
	ds_read_b128 v[218:221], v175 offset:512
	ds_read_b128 v[222:225], v175 offset:33536
	ds_read_b128 v[226:229], v174 offset:576
	v_lshlrev_b32_e32 v147, 16, v97
	v_mul_f32_e32 v149, v149, v149
	s_waitcnt lgkmcnt(4)
	v_mfma_f32_16x16x32_bf16 v[134:137], v[94:97], v[210:213], v[134:137]
	v_fmac_f32_e32 v149, v147, v147
	v_add_f32_e32 v145, v149, v145
	s_waitcnt vmcnt(22)
	v_and_b32_e32 v149, 0xffff0000, v90
	s_waitcnt lgkmcnt(3)
	v_mfma_f32_16x16x32_bf16 v[130:133], v[94:97], v[214:217], v[130:133]
	v_lshlrev_b32_e32 v147, 16, v90
	v_mul_f32_e32 v149, v149, v149
	v_fmac_f32_e32 v149, v147, v147
	s_waitcnt lgkmcnt(2)
	v_mfma_f32_16x16x32_bf16 v[134:137], v[94:97], v[218:221], v[134:137]
	ds_read_b128 v[218:221], v174 offset:33600
	ds_read_b128 v[214:217], v175 offset:33600
	v_add_f32_e32 v145, v149, v145
	v_and_b32_e32 v149, 0xffff0000, v91
	s_waitcnt lgkmcnt(3)
	v_mfma_f32_16x16x32_bf16 v[130:133], v[94:97], v[222:225], v[130:133]
	v_lshlrev_b32_e32 v147, 16, v91
	v_mul_f32_e32 v149, v149, v149
	v_fmac_f32_e32 v149, v147, v147
	v_add_f32_e32 v145, v149, v145
	v_and_b32_e32 v149, 0xffff0000, v92
	ds_read_b128 v[210:213], v175 offset:576
	v_lshlrev_b32_e32 v147, 16, v92
	v_mul_f32_e32 v149, v149, v149
	s_waitcnt lgkmcnt(3)
	v_mfma_f32_16x16x32_bf16 v[134:137], v[90:93], v[226:229], v[134:137]
	v_fmac_f32_e32 v149, v147, v147
	v_add_f32_e32 v145, v149, v145
	v_and_b32_e32 v149, 0xffff0000, v93
	s_waitcnt lgkmcnt(2)
	v_mfma_f32_16x16x32_bf16 v[130:133], v[90:93], v[218:221], v[130:133]
	v_lshlrev_b32_e32 v147, 16, v93
	v_mul_f32_e32 v149, v149, v149
	v_fmac_f32_e32 v149, v147, v147
	s_waitcnt lgkmcnt(0)
	v_mfma_f32_16x16x32_bf16 v[134:137], v[90:93], v[210:213], v[134:137]
	v_add_f32_e32 v145, v149, v145
	v_mfma_f32_16x16x32_bf16 v[130:133], v[90:93], v[214:217], v[130:133]
	s_waitcnt vmcnt(21)
	v_and_b32_e32 v149, 0xffff0000, v86
	v_lshlrev_b32_e32 v147, 16, v86
	v_mul_f32_e32 v149, v149, v149
	v_fmac_f32_e32 v149, v147, v147
	v_add_f32_e32 v145, v149, v145
	v_and_b32_e32 v149, 0xffff0000, v87
	v_lshlrev_b32_e32 v147, 16, v87
	v_mul_f32_e32 v149, v149, v149
	v_fmac_f32_e32 v149, v147, v147
	v_add_f32_e32 v145, v149, v145
	v_and_b32_e32 v149, 0xffff0000, v88
	v_lshlrev_b32_e32 v147, 16, v88
	v_mul_f32_e32 v149, v149, v149
	v_fmac_f32_e32 v149, v147, v147
	v_add_f32_e32 v145, v149, v145
	v_and_b32_e32 v149, 0xffff0000, v89
	ds_read_b128 v[210:213], v174 offset:640
	ds_read_b128 v[214:217], v174 offset:33664
	ds_read_b128 v[218:221], v175 offset:640
	ds_read_b128 v[222:225], v175 offset:33664
	ds_read_b128 v[226:229], v174 offset:704
	v_lshlrev_b32_e32 v147, 16, v89
	v_mul_f32_e32 v149, v149, v149
	s_waitcnt lgkmcnt(4)
	v_mfma_f32_16x16x32_bf16 v[134:137], v[86:89], v[210:213], v[134:137]
	v_fmac_f32_e32 v149, v147, v147
	v_add_f32_e32 v145, v149, v145
	s_waitcnt vmcnt(20)
	v_and_b32_e32 v149, 0xffff0000, v82
	s_waitcnt lgkmcnt(3)
	v_mfma_f32_16x16x32_bf16 v[130:133], v[86:89], v[214:217], v[130:133]
	v_lshlrev_b32_e32 v147, 16, v82
	v_mul_f32_e32 v149, v149, v149
	v_fmac_f32_e32 v149, v147, v147
	s_waitcnt lgkmcnt(2)
	v_mfma_f32_16x16x32_bf16 v[134:137], v[86:89], v[218:221], v[134:137]
	ds_read_b128 v[218:221], v174 offset:33728
	ds_read_b128 v[214:217], v175 offset:33728
	v_add_f32_e32 v145, v149, v145
	v_and_b32_e32 v149, 0xffff0000, v83
	s_waitcnt lgkmcnt(3)
	v_mfma_f32_16x16x32_bf16 v[130:133], v[86:89], v[222:225], v[130:133]
	v_lshlrev_b32_e32 v147, 16, v83
	v_mul_f32_e32 v149, v149, v149
	v_fmac_f32_e32 v149, v147, v147
	v_add_f32_e32 v145, v149, v145
	v_and_b32_e32 v149, 0xffff0000, v84
	ds_read_b128 v[210:213], v175 offset:704
	v_lshlrev_b32_e32 v147, 16, v84
	v_mul_f32_e32 v149, v149, v149
	s_waitcnt lgkmcnt(3)
	v_mfma_f32_16x16x32_bf16 v[134:137], v[82:85], v[226:229], v[134:137]
	v_fmac_f32_e32 v149, v147, v147
	v_add_f32_e32 v145, v149, v145
	v_and_b32_e32 v149, 0xffff0000, v85
	s_waitcnt lgkmcnt(2)
	v_mfma_f32_16x16x32_bf16 v[130:133], v[82:85], v[218:221], v[130:133]
	v_lshlrev_b32_e32 v147, 16, v85
	v_mul_f32_e32 v149, v149, v149
	v_fmac_f32_e32 v149, v147, v147
	s_waitcnt lgkmcnt(0)
	v_mfma_f32_16x16x32_bf16 v[134:137], v[82:85], v[210:213], v[134:137]
	v_add_f32_e32 v145, v149, v145
	v_mfma_f32_16x16x32_bf16 v[130:133], v[82:85], v[214:217], v[130:133]
	s_waitcnt vmcnt(19)
	v_and_b32_e32 v149, 0xffff0000, v78
	v_lshlrev_b32_e32 v147, 16, v78
	v_mul_f32_e32 v149, v149, v149
	v_fmac_f32_e32 v149, v147, v147
	v_add_f32_e32 v145, v149, v145
	v_and_b32_e32 v149, 0xffff0000, v79
	v_lshlrev_b32_e32 v147, 16, v79
	v_mul_f32_e32 v149, v149, v149
	v_fmac_f32_e32 v149, v147, v147
	v_add_f32_e32 v145, v149, v145
	v_and_b32_e32 v149, 0xffff0000, v80
	v_lshlrev_b32_e32 v147, 16, v80
	v_mul_f32_e32 v149, v149, v149
	v_fmac_f32_e32 v149, v147, v147
	v_add_f32_e32 v145, v149, v145
	v_and_b32_e32 v149, 0xffff0000, v81
	ds_read_b128 v[210:213], v174 offset:768
	ds_read_b128 v[214:217], v174 offset:33792
	ds_read_b128 v[218:221], v175 offset:768
	ds_read_b128 v[222:225], v175 offset:33792
	ds_read_b128 v[226:229], v174 offset:832
	v_lshlrev_b32_e32 v147, 16, v81
	v_mul_f32_e32 v149, v149, v149
	s_waitcnt lgkmcnt(4)
	v_mfma_f32_16x16x32_bf16 v[134:137], v[78:81], v[210:213], v[134:137]
	v_fmac_f32_e32 v149, v147, v147
	v_add_f32_e32 v145, v149, v145
	s_waitcnt vmcnt(18)
	v_and_b32_e32 v149, 0xffff0000, v74
	s_waitcnt lgkmcnt(3)
	v_mfma_f32_16x16x32_bf16 v[130:133], v[78:81], v[214:217], v[130:133]
	v_lshlrev_b32_e32 v147, 16, v74
	v_mul_f32_e32 v149, v149, v149
	v_fmac_f32_e32 v149, v147, v147
	s_waitcnt lgkmcnt(2)
	v_mfma_f32_16x16x32_bf16 v[134:137], v[78:81], v[218:221], v[134:137]
	ds_read_b128 v[218:221], v174 offset:33856
	ds_read_b128 v[214:217], v175 offset:33856
	v_add_f32_e32 v145, v149, v145
	v_and_b32_e32 v149, 0xffff0000, v75
	s_waitcnt lgkmcnt(3)
	v_mfma_f32_16x16x32_bf16 v[130:133], v[78:81], v[222:225], v[130:133]
	v_lshlrev_b32_e32 v147, 16, v75
	v_mul_f32_e32 v149, v149, v149
	v_fmac_f32_e32 v149, v147, v147
	v_add_f32_e32 v145, v149, v145
	v_and_b32_e32 v149, 0xffff0000, v76
	ds_read_b128 v[210:213], v175 offset:832
	v_lshlrev_b32_e32 v147, 16, v76
	v_mul_f32_e32 v149, v149, v149
	s_waitcnt lgkmcnt(3)
	v_mfma_f32_16x16x32_bf16 v[134:137], v[74:77], v[226:229], v[134:137]
	v_fmac_f32_e32 v149, v147, v147
	v_add_f32_e32 v145, v149, v145
	v_and_b32_e32 v149, 0xffff0000, v77
	s_waitcnt lgkmcnt(2)
	v_mfma_f32_16x16x32_bf16 v[130:133], v[74:77], v[218:221], v[130:133]
	v_lshlrev_b32_e32 v147, 16, v77
	v_mul_f32_e32 v149, v149, v149
	v_fmac_f32_e32 v149, v147, v147
	s_waitcnt lgkmcnt(0)
	v_mfma_f32_16x16x32_bf16 v[134:137], v[74:77], v[210:213], v[134:137]
	v_add_f32_e32 v145, v149, v145
	v_mfma_f32_16x16x32_bf16 v[130:133], v[74:77], v[214:217], v[130:133]
	s_waitcnt vmcnt(17)
	v_and_b32_e32 v149, 0xffff0000, v70
	v_lshlrev_b32_e32 v147, 16, v70
	v_mul_f32_e32 v149, v149, v149
	v_fmac_f32_e32 v149, v147, v147
	v_add_f32_e32 v145, v149, v145
	v_and_b32_e32 v149, 0xffff0000, v71
	v_lshlrev_b32_e32 v147, 16, v71
	v_mul_f32_e32 v149, v149, v149
	v_fmac_f32_e32 v149, v147, v147
	v_add_f32_e32 v145, v149, v145
	v_and_b32_e32 v149, 0xffff0000, v72
	v_lshlrev_b32_e32 v147, 16, v72
	v_mul_f32_e32 v149, v149, v149
	v_fmac_f32_e32 v149, v147, v147
	v_add_f32_e32 v145, v149, v145
	v_and_b32_e32 v149, 0xffff0000, v73
	ds_read_b128 v[210:213], v174 offset:896
	ds_read_b128 v[214:217], v174 offset:33920
	ds_read_b128 v[218:221], v175 offset:896
	ds_read_b128 v[222:225], v175 offset:33920
	ds_read_b128 v[226:229], v174 offset:960
	v_lshlrev_b32_e32 v147, 16, v73
	v_mul_f32_e32 v149, v149, v149
	s_waitcnt lgkmcnt(4)
	v_mfma_f32_16x16x32_bf16 v[134:137], v[70:73], v[210:213], v[134:137]
	v_fmac_f32_e32 v149, v147, v147
	v_add_f32_e32 v145, v149, v145
	s_waitcnt vmcnt(16)
	v_and_b32_e32 v149, 0xffff0000, v66
	s_waitcnt lgkmcnt(3)
	v_mfma_f32_16x16x32_bf16 v[130:133], v[70:73], v[214:217], v[130:133]
	v_lshlrev_b32_e32 v147, 16, v66
	v_mul_f32_e32 v149, v149, v149
	v_fmac_f32_e32 v149, v147, v147
	s_waitcnt lgkmcnt(2)
	v_mfma_f32_16x16x32_bf16 v[134:137], v[70:73], v[218:221], v[134:137]
	ds_read_b128 v[218:221], v174 offset:33984
	ds_read_b128 v[214:217], v175 offset:33984
	v_add_f32_e32 v145, v149, v145
	v_and_b32_e32 v149, 0xffff0000, v67
	s_waitcnt lgkmcnt(3)
	v_mfma_f32_16x16x32_bf16 v[130:133], v[70:73], v[222:225], v[130:133]
	v_lshlrev_b32_e32 v147, 16, v67
	v_mul_f32_e32 v149, v149, v149
	v_fmac_f32_e32 v149, v147, v147
	v_add_f32_e32 v145, v149, v145
	v_and_b32_e32 v149, 0xffff0000, v68
	ds_read_b128 v[210:213], v175 offset:960
	v_lshlrev_b32_e32 v147, 16, v68
	v_mul_f32_e32 v149, v149, v149
	s_waitcnt lgkmcnt(3)
	v_mfma_f32_16x16x32_bf16 v[134:137], v[66:69], v[226:229], v[134:137]
	v_fmac_f32_e32 v149, v147, v147
	v_add_f32_e32 v145, v149, v145
	v_and_b32_e32 v149, 0xffff0000, v69
	s_waitcnt lgkmcnt(2)
	v_mfma_f32_16x16x32_bf16 v[130:133], v[66:69], v[218:221], v[130:133]
	v_lshlrev_b32_e32 v147, 16, v69
	v_mul_f32_e32 v149, v149, v149
	v_fmac_f32_e32 v149, v147, v147
	s_waitcnt lgkmcnt(0)
	v_mfma_f32_16x16x32_bf16 v[134:137], v[66:69], v[210:213], v[134:137]
	v_add_f32_e32 v145, v149, v145
	v_mfma_f32_16x16x32_bf16 v[130:133], v[66:69], v[214:217], v[130:133]
	s_waitcnt vmcnt(15)
	v_and_b32_e32 v149, 0xffff0000, v62
	v_lshlrev_b32_e32 v147, 16, v62
	v_mul_f32_e32 v149, v149, v149
	v_fmac_f32_e32 v149, v147, v147
	v_add_f32_e32 v145, v149, v145
	v_and_b32_e32 v149, 0xffff0000, v63
	v_lshlrev_b32_e32 v147, 16, v63
	v_mul_f32_e32 v149, v149, v149
	v_fmac_f32_e32 v149, v147, v147
	v_add_f32_e32 v145, v149, v145
	v_and_b32_e32 v149, 0xffff0000, v64
	v_lshlrev_b32_e32 v147, 16, v64
	v_mul_f32_e32 v149, v149, v149
	v_fmac_f32_e32 v149, v147, v147
	v_add_f32_e32 v145, v149, v145
	v_and_b32_e32 v149, 0xffff0000, v65
	ds_read_b128 v[210:213], v174 offset:1024
	ds_read_b128 v[214:217], v174 offset:34048
	ds_read_b128 v[218:221], v175 offset:1024
	ds_read_b128 v[222:225], v175 offset:34048
	ds_read_b128 v[226:229], v174 offset:1088
	v_lshlrev_b32_e32 v147, 16, v65
	v_mul_f32_e32 v149, v149, v149
	s_waitcnt lgkmcnt(4)
	v_mfma_f32_16x16x32_bf16 v[134:137], v[62:65], v[210:213], v[134:137]
	v_fmac_f32_e32 v149, v147, v147
	v_add_f32_e32 v145, v149, v145
	s_waitcnt vmcnt(14)
	v_and_b32_e32 v149, 0xffff0000, v58
	s_waitcnt lgkmcnt(3)
	v_mfma_f32_16x16x32_bf16 v[130:133], v[62:65], v[214:217], v[130:133]
	v_lshlrev_b32_e32 v147, 16, v58
	v_mul_f32_e32 v149, v149, v149
	v_fmac_f32_e32 v149, v147, v147
	s_waitcnt lgkmcnt(2)
	v_mfma_f32_16x16x32_bf16 v[134:137], v[62:65], v[218:221], v[134:137]
	ds_read_b128 v[218:221], v174 offset:34112
	ds_read_b128 v[214:217], v175 offset:34112
	v_add_f32_e32 v145, v149, v145
	v_and_b32_e32 v149, 0xffff0000, v59
	s_waitcnt lgkmcnt(3)
	v_mfma_f32_16x16x32_bf16 v[130:133], v[62:65], v[222:225], v[130:133]
	v_lshlrev_b32_e32 v147, 16, v59
	v_mul_f32_e32 v149, v149, v149
	v_fmac_f32_e32 v149, v147, v147
	v_add_f32_e32 v145, v149, v145
	v_and_b32_e32 v149, 0xffff0000, v60
	ds_read_b128 v[210:213], v175 offset:1088
	v_lshlrev_b32_e32 v147, 16, v60
	v_mul_f32_e32 v149, v149, v149
	s_waitcnt lgkmcnt(3)
	v_mfma_f32_16x16x32_bf16 v[134:137], v[58:61], v[226:229], v[134:137]
	v_fmac_f32_e32 v149, v147, v147
	v_add_f32_e32 v145, v149, v145
	v_and_b32_e32 v149, 0xffff0000, v61
	s_waitcnt lgkmcnt(2)
	v_mfma_f32_16x16x32_bf16 v[130:133], v[58:61], v[218:221], v[130:133]
	v_lshlrev_b32_e32 v147, 16, v61
	v_mul_f32_e32 v149, v149, v149
	v_fmac_f32_e32 v149, v147, v147
	s_waitcnt lgkmcnt(0)
	v_mfma_f32_16x16x32_bf16 v[134:137], v[58:61], v[210:213], v[134:137]
	v_add_f32_e32 v145, v149, v145
	v_mfma_f32_16x16x32_bf16 v[130:133], v[58:61], v[214:217], v[130:133]
	s_waitcnt vmcnt(13)
	v_and_b32_e32 v149, 0xffff0000, v54
	v_lshlrev_b32_e32 v147, 16, v54
	v_mul_f32_e32 v149, v149, v149
	v_fmac_f32_e32 v149, v147, v147
	v_add_f32_e32 v145, v149, v145
	v_and_b32_e32 v149, 0xffff0000, v55
	v_lshlrev_b32_e32 v147, 16, v55
	v_mul_f32_e32 v149, v149, v149
	v_fmac_f32_e32 v149, v147, v147
	v_add_f32_e32 v145, v149, v145
	v_and_b32_e32 v149, 0xffff0000, v56
	v_lshlrev_b32_e32 v147, 16, v56
	v_mul_f32_e32 v149, v149, v149
	v_fmac_f32_e32 v149, v147, v147
	v_add_f32_e32 v145, v149, v145
	v_and_b32_e32 v149, 0xffff0000, v57
	ds_read_b128 v[210:213], v174 offset:1152
	ds_read_b128 v[214:217], v174 offset:34176
	ds_read_b128 v[218:221], v175 offset:1152
	ds_read_b128 v[222:225], v175 offset:34176
	ds_read_b128 v[226:229], v174 offset:1216
	v_lshlrev_b32_e32 v147, 16, v57
	v_mul_f32_e32 v149, v149, v149
	s_waitcnt lgkmcnt(4)
	v_mfma_f32_16x16x32_bf16 v[134:137], v[54:57], v[210:213], v[134:137]
	v_fmac_f32_e32 v149, v147, v147
	v_add_f32_e32 v145, v149, v145
	s_waitcnt vmcnt(12)
	v_and_b32_e32 v149, 0xffff0000, v50
	s_waitcnt lgkmcnt(3)
	v_mfma_f32_16x16x32_bf16 v[130:133], v[54:57], v[214:217], v[130:133]
	v_lshlrev_b32_e32 v147, 16, v50
	v_mul_f32_e32 v149, v149, v149
	v_fmac_f32_e32 v149, v147, v147
	s_waitcnt lgkmcnt(2)
	v_mfma_f32_16x16x32_bf16 v[134:137], v[54:57], v[218:221], v[134:137]
	ds_read_b128 v[218:221], v174 offset:34240
	ds_read_b128 v[214:217], v175 offset:34240
	v_add_f32_e32 v145, v149, v145
	v_and_b32_e32 v149, 0xffff0000, v51
	s_waitcnt lgkmcnt(3)
	v_mfma_f32_16x16x32_bf16 v[130:133], v[54:57], v[222:225], v[130:133]
	v_lshlrev_b32_e32 v147, 16, v51
	v_mul_f32_e32 v149, v149, v149
	v_fmac_f32_e32 v149, v147, v147
	v_add_f32_e32 v145, v149, v145
	v_and_b32_e32 v149, 0xffff0000, v52
	ds_read_b128 v[210:213], v175 offset:1216
	v_lshlrev_b32_e32 v147, 16, v52
	v_mul_f32_e32 v149, v149, v149
	s_waitcnt lgkmcnt(3)
	v_mfma_f32_16x16x32_bf16 v[134:137], v[50:53], v[226:229], v[134:137]
	v_fmac_f32_e32 v149, v147, v147
	v_add_f32_e32 v145, v149, v145
	v_and_b32_e32 v149, 0xffff0000, v53
	s_waitcnt lgkmcnt(2)
	v_mfma_f32_16x16x32_bf16 v[130:133], v[50:53], v[218:221], v[130:133]
	v_lshlrev_b32_e32 v147, 16, v53
	v_mul_f32_e32 v149, v149, v149
	v_fmac_f32_e32 v149, v147, v147
	s_waitcnt lgkmcnt(0)
	v_mfma_f32_16x16x32_bf16 v[134:137], v[50:53], v[210:213], v[134:137]
	v_add_f32_e32 v145, v149, v145
	v_mfma_f32_16x16x32_bf16 v[130:133], v[50:53], v[214:217], v[130:133]
	s_waitcnt vmcnt(11)
	v_and_b32_e32 v149, 0xffff0000, v46
	v_lshlrev_b32_e32 v147, 16, v46
	v_mul_f32_e32 v149, v149, v149
	v_fmac_f32_e32 v149, v147, v147
	v_add_f32_e32 v145, v149, v145
	v_and_b32_e32 v149, 0xffff0000, v47
	v_lshlrev_b32_e32 v147, 16, v47
	v_mul_f32_e32 v149, v149, v149
	v_fmac_f32_e32 v149, v147, v147
	v_add_f32_e32 v145, v149, v145
	v_and_b32_e32 v149, 0xffff0000, v48
	v_lshlrev_b32_e32 v147, 16, v48
	v_mul_f32_e32 v149, v149, v149
	v_fmac_f32_e32 v149, v147, v147
	v_add_f32_e32 v145, v149, v145
	v_and_b32_e32 v149, 0xffff0000, v49
	ds_read_b128 v[210:213], v174 offset:1280
	ds_read_b128 v[214:217], v174 offset:34304
	ds_read_b128 v[218:221], v175 offset:1280
	ds_read_b128 v[222:225], v175 offset:34304
	ds_read_b128 v[226:229], v174 offset:1344
	v_lshlrev_b32_e32 v147, 16, v49
	v_mul_f32_e32 v149, v149, v149
	s_waitcnt lgkmcnt(4)
	v_mfma_f32_16x16x32_bf16 v[134:137], v[46:49], v[210:213], v[134:137]
	v_fmac_f32_e32 v149, v147, v147
	v_add_f32_e32 v145, v149, v145
	s_waitcnt vmcnt(10)
	v_and_b32_e32 v149, 0xffff0000, v42
	s_waitcnt lgkmcnt(3)
	v_mfma_f32_16x16x32_bf16 v[130:133], v[46:49], v[214:217], v[130:133]
	v_lshlrev_b32_e32 v147, 16, v42
	v_mul_f32_e32 v149, v149, v149
	v_fmac_f32_e32 v149, v147, v147
	s_waitcnt lgkmcnt(2)
	v_mfma_f32_16x16x32_bf16 v[134:137], v[46:49], v[218:221], v[134:137]
	ds_read_b128 v[218:221], v174 offset:34368
	ds_read_b128 v[214:217], v175 offset:34368
	v_add_f32_e32 v145, v149, v145
	v_and_b32_e32 v149, 0xffff0000, v43
	s_waitcnt lgkmcnt(3)
	v_mfma_f32_16x16x32_bf16 v[130:133], v[46:49], v[222:225], v[130:133]
	v_lshlrev_b32_e32 v147, 16, v43
	v_mul_f32_e32 v149, v149, v149
	v_fmac_f32_e32 v149, v147, v147
	v_add_f32_e32 v145, v149, v145
	v_and_b32_e32 v149, 0xffff0000, v44
	ds_read_b128 v[210:213], v175 offset:1344
	v_lshlrev_b32_e32 v147, 16, v44
	v_mul_f32_e32 v149, v149, v149
	s_waitcnt lgkmcnt(3)
	v_mfma_f32_16x16x32_bf16 v[134:137], v[42:45], v[226:229], v[134:137]
	v_fmac_f32_e32 v149, v147, v147
	v_add_f32_e32 v145, v149, v145
	v_and_b32_e32 v149, 0xffff0000, v45
	s_waitcnt lgkmcnt(2)
	v_mfma_f32_16x16x32_bf16 v[130:133], v[42:45], v[218:221], v[130:133]
	v_lshlrev_b32_e32 v147, 16, v45
	v_mul_f32_e32 v149, v149, v149
	v_fmac_f32_e32 v149, v147, v147
	s_waitcnt lgkmcnt(0)
	v_mfma_f32_16x16x32_bf16 v[134:137], v[42:45], v[210:213], v[134:137]
	v_add_f32_e32 v145, v149, v145
	v_mfma_f32_16x16x32_bf16 v[130:133], v[42:45], v[214:217], v[130:133]
	s_waitcnt vmcnt(9)
	v_and_b32_e32 v149, 0xffff0000, v38
	v_lshlrev_b32_e32 v147, 16, v38
	v_mul_f32_e32 v149, v149, v149
	v_fmac_f32_e32 v149, v147, v147
	v_add_f32_e32 v145, v149, v145
	v_and_b32_e32 v149, 0xffff0000, v39
	v_lshlrev_b32_e32 v147, 16, v39
	v_mul_f32_e32 v149, v149, v149
	v_fmac_f32_e32 v149, v147, v147
	v_add_f32_e32 v145, v149, v145
	v_and_b32_e32 v149, 0xffff0000, v40
	v_lshlrev_b32_e32 v147, 16, v40
	v_mul_f32_e32 v149, v149, v149
	v_fmac_f32_e32 v149, v147, v147
	v_add_f32_e32 v145, v149, v145
	v_and_b32_e32 v149, 0xffff0000, v41
	ds_read_b128 v[210:213], v174 offset:1408
	ds_read_b128 v[214:217], v174 offset:34432
	ds_read_b128 v[218:221], v175 offset:1408
	ds_read_b128 v[222:225], v175 offset:34432
	ds_read_b128 v[226:229], v174 offset:1472
	v_lshlrev_b32_e32 v147, 16, v41
	v_mul_f32_e32 v149, v149, v149
	s_waitcnt lgkmcnt(4)
	v_mfma_f32_16x16x32_bf16 v[134:137], v[38:41], v[210:213], v[134:137]
	v_fmac_f32_e32 v149, v147, v147
	v_add_f32_e32 v145, v149, v145
	s_waitcnt vmcnt(8)
	v_and_b32_e32 v149, 0xffff0000, v34
	s_waitcnt lgkmcnt(3)
	v_mfma_f32_16x16x32_bf16 v[130:133], v[38:41], v[214:217], v[130:133]
	v_lshlrev_b32_e32 v147, 16, v34
	v_mul_f32_e32 v149, v149, v149
	v_fmac_f32_e32 v149, v147, v147
	s_waitcnt lgkmcnt(2)
	v_mfma_f32_16x16x32_bf16 v[134:137], v[38:41], v[218:221], v[134:137]
	ds_read_b128 v[218:221], v174 offset:34496
	ds_read_b128 v[214:217], v175 offset:34496
	v_add_f32_e32 v145, v149, v145
	v_and_b32_e32 v149, 0xffff0000, v35
	s_waitcnt lgkmcnt(3)
	v_mfma_f32_16x16x32_bf16 v[130:133], v[38:41], v[222:225], v[130:133]
	v_lshlrev_b32_e32 v147, 16, v35
	v_mul_f32_e32 v149, v149, v149
	v_fmac_f32_e32 v149, v147, v147
	v_add_f32_e32 v145, v149, v145
	v_and_b32_e32 v149, 0xffff0000, v36
	ds_read_b128 v[210:213], v175 offset:1472
	v_lshlrev_b32_e32 v147, 16, v36
	v_mul_f32_e32 v149, v149, v149
	s_waitcnt lgkmcnt(3)
	v_mfma_f32_16x16x32_bf16 v[134:137], v[34:37], v[226:229], v[134:137]
	v_fmac_f32_e32 v149, v147, v147
	v_add_f32_e32 v145, v149, v145
	v_and_b32_e32 v149, 0xffff0000, v37
	s_waitcnt lgkmcnt(2)
	v_mfma_f32_16x16x32_bf16 v[130:133], v[34:37], v[218:221], v[130:133]
	v_lshlrev_b32_e32 v147, 16, v37
	v_mul_f32_e32 v149, v149, v149
	v_fmac_f32_e32 v149, v147, v147
	s_waitcnt lgkmcnt(0)
	v_mfma_f32_16x16x32_bf16 v[134:137], v[34:37], v[210:213], v[134:137]
	v_add_f32_e32 v145, v149, v145
	v_mfma_f32_16x16x32_bf16 v[130:133], v[34:37], v[214:217], v[130:133]
	s_waitcnt vmcnt(7)
	v_and_b32_e32 v149, 0xffff0000, v30
	v_lshlrev_b32_e32 v147, 16, v30
	v_mul_f32_e32 v149, v149, v149
	v_fmac_f32_e32 v149, v147, v147
	v_add_f32_e32 v145, v149, v145
	v_and_b32_e32 v149, 0xffff0000, v31
	v_lshlrev_b32_e32 v147, 16, v31
	v_mul_f32_e32 v149, v149, v149
	v_fmac_f32_e32 v149, v147, v147
	v_add_f32_e32 v145, v149, v145
	v_and_b32_e32 v149, 0xffff0000, v32
	v_lshlrev_b32_e32 v147, 16, v32
	v_mul_f32_e32 v149, v149, v149
	v_fmac_f32_e32 v149, v147, v147
	v_add_f32_e32 v145, v149, v145
	v_and_b32_e32 v149, 0xffff0000, v33
	ds_read_b128 v[210:213], v174 offset:1536
	ds_read_b128 v[214:217], v174 offset:34560
	ds_read_b128 v[218:221], v175 offset:1536
	ds_read_b128 v[222:225], v175 offset:34560
	ds_read_b128 v[226:229], v174 offset:1600
	v_lshlrev_b32_e32 v147, 16, v33
	v_mul_f32_e32 v149, v149, v149
	s_waitcnt lgkmcnt(4)
	v_mfma_f32_16x16x32_bf16 v[134:137], v[30:33], v[210:213], v[134:137]
	v_fmac_f32_e32 v149, v147, v147
	v_add_f32_e32 v145, v149, v145
	s_waitcnt vmcnt(6)
	v_and_b32_e32 v149, 0xffff0000, v26
	s_waitcnt lgkmcnt(3)
	v_mfma_f32_16x16x32_bf16 v[130:133], v[30:33], v[214:217], v[130:133]
	v_lshlrev_b32_e32 v147, 16, v26
	v_mul_f32_e32 v149, v149, v149
	v_fmac_f32_e32 v149, v147, v147
	s_waitcnt lgkmcnt(2)
	v_mfma_f32_16x16x32_bf16 v[134:137], v[30:33], v[218:221], v[134:137]
	ds_read_b128 v[218:221], v174 offset:34624
	ds_read_b128 v[214:217], v175 offset:34624
	v_add_f32_e32 v145, v149, v145
	v_and_b32_e32 v149, 0xffff0000, v27
	s_waitcnt lgkmcnt(3)
	v_mfma_f32_16x16x32_bf16 v[130:133], v[30:33], v[222:225], v[130:133]
	v_lshlrev_b32_e32 v147, 16, v27
	v_mul_f32_e32 v149, v149, v149
	v_fmac_f32_e32 v149, v147, v147
	v_add_f32_e32 v145, v149, v145
	v_and_b32_e32 v149, 0xffff0000, v28
	ds_read_b128 v[210:213], v175 offset:1600
	v_lshlrev_b32_e32 v147, 16, v28
	v_mul_f32_e32 v149, v149, v149
	s_waitcnt lgkmcnt(3)
	v_mfma_f32_16x16x32_bf16 v[134:137], v[26:29], v[226:229], v[134:137]
	v_fmac_f32_e32 v149, v147, v147
	v_add_f32_e32 v145, v149, v145
	v_and_b32_e32 v149, 0xffff0000, v29
	s_waitcnt lgkmcnt(2)
	v_mfma_f32_16x16x32_bf16 v[130:133], v[26:29], v[218:221], v[130:133]
	v_lshlrev_b32_e32 v147, 16, v29
	v_mul_f32_e32 v149, v149, v149
	v_fmac_f32_e32 v149, v147, v147
	s_waitcnt lgkmcnt(0)
	v_mfma_f32_16x16x32_bf16 v[134:137], v[26:29], v[210:213], v[134:137]
	v_add_f32_e32 v145, v149, v145
	v_mfma_f32_16x16x32_bf16 v[130:133], v[26:29], v[214:217], v[130:133]
	s_waitcnt vmcnt(5)
	v_and_b32_e32 v149, 0xffff0000, v22
	v_lshlrev_b32_e32 v147, 16, v22
	v_mul_f32_e32 v149, v149, v149
	v_fmac_f32_e32 v149, v147, v147
	v_add_f32_e32 v145, v149, v145
	v_and_b32_e32 v149, 0xffff0000, v23
	v_lshlrev_b32_e32 v147, 16, v23
	v_mul_f32_e32 v149, v149, v149
	v_fmac_f32_e32 v149, v147, v147
	v_add_f32_e32 v145, v149, v145
	v_and_b32_e32 v149, 0xffff0000, v24
	v_lshlrev_b32_e32 v147, 16, v24
	v_mul_f32_e32 v149, v149, v149
	v_fmac_f32_e32 v149, v147, v147
	v_add_f32_e32 v145, v149, v145
	v_and_b32_e32 v149, 0xffff0000, v25
	ds_read_b128 v[210:213], v174 offset:1664
	ds_read_b128 v[214:217], v174 offset:34688
	ds_read_b128 v[218:221], v175 offset:1664
	ds_read_b128 v[222:225], v175 offset:34688
	ds_read_b128 v[226:229], v174 offset:1728
	v_lshlrev_b32_e32 v147, 16, v25
	v_mul_f32_e32 v149, v149, v149
	s_waitcnt lgkmcnt(4)
	v_mfma_f32_16x16x32_bf16 v[134:137], v[22:25], v[210:213], v[134:137]
	v_fmac_f32_e32 v149, v147, v147
	v_add_f32_e32 v145, v149, v145
	s_waitcnt vmcnt(4)
	v_and_b32_e32 v149, 0xffff0000, v18
	s_waitcnt lgkmcnt(3)
	v_mfma_f32_16x16x32_bf16 v[130:133], v[22:25], v[214:217], v[130:133]
	v_lshlrev_b32_e32 v147, 16, v18
	v_mul_f32_e32 v149, v149, v149
	v_fmac_f32_e32 v149, v147, v147
	s_waitcnt lgkmcnt(2)
	v_mfma_f32_16x16x32_bf16 v[134:137], v[22:25], v[218:221], v[134:137]
	ds_read_b128 v[218:221], v174 offset:34752
	ds_read_b128 v[214:217], v175 offset:34752
	v_add_f32_e32 v145, v149, v145
	v_and_b32_e32 v149, 0xffff0000, v19
	s_waitcnt lgkmcnt(3)
	v_mfma_f32_16x16x32_bf16 v[130:133], v[22:25], v[222:225], v[130:133]
	v_lshlrev_b32_e32 v147, 16, v19
	v_mul_f32_e32 v149, v149, v149
	v_fmac_f32_e32 v149, v147, v147
	v_add_f32_e32 v145, v149, v145
	v_and_b32_e32 v149, 0xffff0000, v20
	ds_read_b128 v[210:213], v175 offset:1728
	v_lshlrev_b32_e32 v147, 16, v20
	v_mul_f32_e32 v149, v149, v149
	s_waitcnt lgkmcnt(3)
	v_mfma_f32_16x16x32_bf16 v[134:137], v[18:21], v[226:229], v[134:137]
	v_fmac_f32_e32 v149, v147, v147
	v_add_f32_e32 v145, v149, v145
	v_and_b32_e32 v149, 0xffff0000, v21
	s_waitcnt lgkmcnt(2)
	v_mfma_f32_16x16x32_bf16 v[130:133], v[18:21], v[218:221], v[130:133]
	v_lshlrev_b32_e32 v147, 16, v21
	v_mul_f32_e32 v149, v149, v149
	v_fmac_f32_e32 v149, v147, v147
	s_waitcnt lgkmcnt(0)
	v_mfma_f32_16x16x32_bf16 v[134:137], v[18:21], v[210:213], v[134:137]
	v_add_f32_e32 v145, v149, v145
	v_mfma_f32_16x16x32_bf16 v[130:133], v[18:21], v[214:217], v[130:133]
	s_waitcnt vmcnt(3)
	v_and_b32_e32 v149, 0xffff0000, v14
	v_lshlrev_b32_e32 v147, 16, v14
	v_mul_f32_e32 v149, v149, v149
	v_fmac_f32_e32 v149, v147, v147
	v_add_f32_e32 v145, v149, v145
	v_and_b32_e32 v149, 0xffff0000, v15
	v_lshlrev_b32_e32 v147, 16, v15
	v_mul_f32_e32 v149, v149, v149
	v_fmac_f32_e32 v149, v147, v147
	v_add_f32_e32 v145, v149, v145
	v_and_b32_e32 v149, 0xffff0000, v16
	v_lshlrev_b32_e32 v147, 16, v16
	v_mul_f32_e32 v149, v149, v149
	v_fmac_f32_e32 v149, v147, v147
	v_add_f32_e32 v145, v149, v145
	v_and_b32_e32 v149, 0xffff0000, v17
	ds_read_b128 v[210:213], v174 offset:1792
	ds_read_b128 v[214:217], v174 offset:34816
	ds_read_b128 v[218:221], v175 offset:1792
	ds_read_b128 v[222:225], v175 offset:34816
	ds_read_b128 v[226:229], v174 offset:1856
	v_lshlrev_b32_e32 v147, 16, v17
	v_mul_f32_e32 v149, v149, v149
	s_waitcnt lgkmcnt(4)
	v_mfma_f32_16x16x32_bf16 v[134:137], v[14:17], v[210:213], v[134:137]
	v_fmac_f32_e32 v149, v147, v147
	v_add_f32_e32 v145, v149, v145
	s_waitcnt vmcnt(2)
	v_and_b32_e32 v149, 0xffff0000, v10
	s_waitcnt lgkmcnt(3)
	v_mfma_f32_16x16x32_bf16 v[130:133], v[14:17], v[214:217], v[130:133]
	v_lshlrev_b32_e32 v147, 16, v10
	v_mul_f32_e32 v149, v149, v149
	v_fmac_f32_e32 v149, v147, v147
	s_waitcnt lgkmcnt(2)
	v_mfma_f32_16x16x32_bf16 v[134:137], v[14:17], v[218:221], v[134:137]
	ds_read_b128 v[218:221], v174 offset:34880
	ds_read_b128 v[214:217], v175 offset:34880
	v_add_f32_e32 v145, v149, v145
	v_and_b32_e32 v149, 0xffff0000, v11
	s_waitcnt lgkmcnt(3)
	v_mfma_f32_16x16x32_bf16 v[130:133], v[14:17], v[222:225], v[130:133]
	v_lshlrev_b32_e32 v147, 16, v11
	v_mul_f32_e32 v149, v149, v149
	v_fmac_f32_e32 v149, v147, v147
	v_add_f32_e32 v145, v149, v145
	v_and_b32_e32 v149, 0xffff0000, v12
	ds_read_b128 v[210:213], v175 offset:1856
	v_lshlrev_b32_e32 v147, 16, v12
	v_mul_f32_e32 v149, v149, v149
	s_waitcnt lgkmcnt(3)
	v_mfma_f32_16x16x32_bf16 v[134:137], v[10:13], v[226:229], v[134:137]
	v_fmac_f32_e32 v149, v147, v147
	v_add_f32_e32 v145, v149, v145
	v_and_b32_e32 v149, 0xffff0000, v13
	s_waitcnt lgkmcnt(2)
	v_mfma_f32_16x16x32_bf16 v[130:133], v[10:13], v[218:221], v[130:133]
	v_lshlrev_b32_e32 v147, 16, v13
	v_mul_f32_e32 v149, v149, v149
	v_fmac_f32_e32 v149, v147, v147
	s_waitcnt lgkmcnt(0)
	v_mfma_f32_16x16x32_bf16 v[134:137], v[10:13], v[210:213], v[134:137]
	v_add_f32_e32 v145, v149, v145
	v_mfma_f32_16x16x32_bf16 v[130:133], v[10:13], v[214:217], v[130:133]
	s_waitcnt vmcnt(1)
	v_and_b32_e32 v149, 0xffff0000, v6
	ds_read_b128 v[210:213], v174 offset:1920
	ds_read_b128 v[214:217], v174 offset:34944
	ds_read_b128 v[218:221], v175 offset:1920
	ds_read_b128 v[222:225], v175 offset:34944
	ds_read_b128 v[226:229], v174 offset:1984
	v_lshlrev_b32_e32 v147, 16, v6
	v_mul_f32_e32 v149, v149, v149
	s_waitcnt lgkmcnt(4)
	v_mfma_f32_16x16x32_bf16 v[134:137], v[6:9], v[210:213], v[134:137]
	v_fmac_f32_e32 v149, v147, v147
	v_add_f32_e32 v145, v149, v145
	v_and_b32_e32 v149, 0xffff0000, v7
	v_lshlrev_b32_e32 v147, 16, v7
	v_mul_f32_e32 v149, v149, v149
	v_fmac_f32_e32 v149, v147, v147
	s_waitcnt lgkmcnt(2)
	v_mfma_f32_16x16x32_bf16 v[134:137], v[6:9], v[218:221], v[134:137]
	v_add_f32_e32 v145, v149, v145
	v_and_b32_e32 v149, 0xffff0000, v8
	v_lshlrev_b32_e32 v147, 16, v8
	v_mfma_f32_16x16x32_bf16 v[130:133], v[6:9], v[214:217], v[130:133]
	v_mul_f32_e32 v149, v149, v149
	v_fmac_f32_e32 v149, v147, v147
	v_add_f32_e32 v145, v149, v145
	v_and_b32_e32 v149, 0xffff0000, v9
	s_waitcnt lgkmcnt(1)
	v_mfma_f32_16x16x32_bf16 v[222:225], v[6:9], v[222:225], v[130:133]
	v_lshlrev_b32_e32 v147, 16, v9
	ds_read_b128 v[218:221], v174 offset:35008
	ds_read_b128 v[214:217], v175 offset:35008
	s_waitcnt vmcnt(0) lgkmcnt(2)
	v_mfma_f32_16x16x32_bf16 v[130:133], v[2:5], v[226:229], v[134:137]
	ds_read_b128 v[210:213], v175 offset:1984
	s_nop 1
	v_mul_f32_e32 v134, v149, v149
	v_and_b32_e32 v136, 0xffff0000, v2
	v_fmac_f32_e32 v134, v147, v147
	v_lshlrev_b32_e32 v135, 16, v2
	v_mul_f32_e32 v136, v136, v136
	v_add_f32_e32 v134, v134, v145
	v_fmac_f32_e32 v136, v135, v135
	v_add_f32_e32 v134, v136, v134
	v_and_b32_e32 v136, 0xffff0000, v3
	v_lshlrev_b32_e32 v135, 16, v3
	v_mul_f32_e32 v136, v136, v136
	v_fmac_f32_e32 v136, v135, v135
	v_add_f32_e32 v134, v136, v134
	v_and_b32_e32 v136, 0xffff0000, v4
	v_lshlrev_b32_e32 v135, 16, v4
	v_mul_f32_e32 v136, v136, v136
	v_fmac_f32_e32 v136, v135, v135
	v_add_f32_e32 v145, v136, v134
	s_waitcnt lgkmcnt(2)
	v_mfma_f32_16x16x32_bf16 v[134:137], v[2:5], v[218:221], v[222:225]
	v_and_b32_e32 v149, 0xffff0000, v5
	v_lshlrev_b32_e32 v147, 16, v5
	v_mul_f32_e32 v149, v149, v149
	v_fmac_f32_e32 v149, v147, v147
	s_waitcnt lgkmcnt(0)
	v_mfma_f32_16x16x32_bf16 v[130:133], v[2:5], v[210:213], v[130:133]
	v_add_f32_e32 v145, v149, v145
	v_mfma_f32_16x16x32_bf16 v[134:137], v[2:5], v[214:217], v[134:137]
	ds_bpermute_b32 v147, v192, v145
	v_lshlrev_b32_e32 v149, 16, v126
	v_and_b32_e32 v126, 0xffff0000, v126
	s_waitcnt lgkmcnt(0)
	v_add_f32_e32 v145, v145, v147
	ds_bpermute_b32 v147, v193, v145
	s_waitcnt lgkmcnt(0)
	v_add_f32_e32 v145, v145, v147
	v_fmamk_f32 v145, v145, 0x3a800000, v195
	v_mul_f32_e32 v147, 0x4f800000, v145
	v_cmp_gt_f32_e32 vcc, s25, v145
	s_nop 1
	v_cndmask_b32_e32 v145, v145, v147, vcc
	v_sqrt_f32_e32 v147, v145
	s_nop 0
	v_add_u32_e32 v151, -1, v147
	v_add_u32_e32 v153, 1, v147
	v_fma_f32 v155, -v151, v147, v145
	v_fma_f32 v157, -v153, v147, v145
	v_cmp_ge_f32_e64 s[8:9], 0, v155
	s_nop 1
	v_cndmask_b32_e64 v147, v147, v151, s[8:9]
	v_cmp_lt_f32_e64 s[8:9], 0, v157
	s_nop 1
	v_cndmask_b32_e64 v147, v147, v153, s[8:9]
	v_mul_f32_e32 v151, 0x37800000, v147
	v_cndmask_b32_e32 v147, v147, v151, vcc
	v_cmp_class_f32_e32 vcc, v145, v196
	s_nop 1
	v_cndmask_b32_e32 v145, v147, v145, vcc
	v_div_scale_f32 v147, s[8:9], v145, v145, 1.0
	v_rcp_f32_e32 v151, v147
	v_div_scale_f32 v153, vcc, 1.0, v145, 1.0
	v_fma_f32 v155, -v147, v151, 1.0
	v_fmac_f32_e32 v151, v155, v151
	v_mul_f32_e32 v155, v153, v151
	v_fma_f32 v157, -v147, v155, v153
	v_fmac_f32_e32 v155, v157, v151
	v_fma_f32 v147, -v147, v155, v153
	v_div_fmas_f32 v147, v147, v151, v155
	v_div_fixup_f32 v145, v147, v145, 1.0
	v_mul_f32_e32 v147, 0x41800000, v145
	v_mul_f32_e32 v149, v147, v149
	v_mul_f32_e32 v126, v147, v126
	v_cvt_pk_fp8_f32 v210, v149, v126
	v_lshlrev_b32_e32 v151, 16, v127
	v_and_b32_e32 v127, 0xffff0000, v127
	v_mul_f32_e32 v126, v147, v151
	v_mul_f32_e32 v127, v147, v127
	v_cvt_pk_fp8_f32 v210, v126, v127 op_sel:[0,0,1]
	v_lshlrev_b32_e32 v126, 16, v128
	v_and_b32_e32 v127, 0xffff0000, v128
	v_mul_f32_e32 v126, v147, v126
	v_mul_f32_e32 v127, v147, v127
	v_cvt_pk_fp8_f32 v211, v126, v127
	v_lshlrev_b32_e32 v128, 16, v129
	v_and_b32_e32 v127, 0xffff0000, v129
	v_mul_f32_e32 v126, v147, v128
	v_mul_f32_e32 v127, v147, v127
	v_cvt_pk_fp8_f32 v211, v126, v127 op_sel:[0,0,1]
	v_lshl_add_u64 v[126:127], v[142:143], 0, v[168:169]
	global_store_dwordx2 v[126:127], v[210:211], off
	s_nop 0
	v_lshlrev_b32_e32 v128, 16, v122
	v_and_b32_e32 v122, 0xffff0000, v122
	v_mul_f32_e32 v128, v147, v128
	v_mul_f32_e32 v129, v147, v122
	v_cvt_pk_fp8_f32 v122, v128, v129
	v_lshlrev_b32_e32 v149, 16, v123
	v_and_b32_e32 v123, 0xffff0000, v123
	v_mul_f32_e32 v128, v147, v149
	v_mul_f32_e32 v123, v147, v123
	v_cvt_pk_fp8_f32 v122, v128, v123 op_sel:[0,0,1]
	v_lshlrev_b32_e32 v123, 16, v124
	v_mul_f32_e32 v128, v147, v123
	v_and_b32_e32 v123, 0xffff0000, v124
	v_mul_f32_e32 v124, v147, v123
	v_cvt_pk_fp8_f32 v123, v128, v124
	v_lshlrev_b32_e32 v129, 16, v125
	v_and_b32_e32 v125, 0xffff0000, v125
	v_mul_f32_e32 v124, v147, v129
	v_mul_f32_e32 v125, v147, v125
	v_cvt_pk_fp8_f32 v123, v124, v125 op_sel:[0,0,1]
	global_store_dwordx2 v[126:127], v[122:123], off offset:32
	s_nop 0
	v_lshlrev_b32_e32 v122, 16, v118
	v_and_b32_e32 v118, 0xffff0000, v118
	v_mul_f32_e32 v122, v147, v122
	v_mul_f32_e32 v123, v147, v118
	v_cvt_pk_fp8_f32 v118, v122, v123
	v_lshlrev_b32_e32 v124, 16, v119
	v_and_b32_e32 v119, 0xffff0000, v119
	v_mul_f32_e32 v122, v147, v124
	v_mul_f32_e32 v119, v147, v119
	v_cvt_pk_fp8_f32 v118, v122, v119 op_sel:[0,0,1]
	v_lshlrev_b32_e32 v119, 16, v120
	v_mul_f32_e32 v122, v147, v119
	v_and_b32_e32 v119, 0xffff0000, v120
	v_mul_f32_e32 v120, v147, v119
	v_cvt_pk_fp8_f32 v119, v122, v120
	v_lshlrev_b32_e32 v123, 16, v121
	v_and_b32_e32 v121, 0xffff0000, v121
	v_mul_f32_e32 v120, v147, v123
	v_mul_f32_e32 v121, v147, v121
	v_cvt_pk_fp8_f32 v119, v120, v121 op_sel:[0,0,1]
	global_store_dwordx2 v[126:127], v[118:119], off offset:64
	s_nop 0
	v_lshlrev_b32_e32 v118, 16, v114
	v_and_b32_e32 v114, 0xffff0000, v114
	v_mul_f32_e32 v118, v147, v118
	v_mul_f32_e32 v119, v147, v114
	v_cvt_pk_fp8_f32 v114, v118, v119
	v_lshlrev_b32_e32 v120, 16, v115
	v_and_b32_e32 v115, 0xffff0000, v115
	v_mul_f32_e32 v118, v147, v120
	v_mul_f32_e32 v115, v147, v115
	v_cvt_pk_fp8_f32 v114, v118, v115 op_sel:[0,0,1]
	v_lshlrev_b32_e32 v115, 16, v116
	v_mul_f32_e32 v118, v147, v115
	v_and_b32_e32 v115, 0xffff0000, v116
	v_mul_f32_e32 v116, v147, v115
	v_cvt_pk_fp8_f32 v115, v118, v116
	v_lshlrev_b32_e32 v119, 16, v117
	v_and_b32_e32 v117, 0xffff0000, v117
	v_mul_f32_e32 v116, v147, v119
	v_mul_f32_e32 v117, v147, v117
	v_cvt_pk_fp8_f32 v115, v116, v117 op_sel:[0,0,1]
	global_store_dwordx2 v[126:127], v[114:115], off offset:96
	s_nop 0
	v_lshlrev_b32_e32 v114, 16, v110
	v_and_b32_e32 v110, 0xffff0000, v110
	v_mul_f32_e32 v114, v147, v114
	v_mul_f32_e32 v115, v147, v110
	v_cvt_pk_fp8_f32 v110, v114, v115
	v_lshlrev_b32_e32 v116, 16, v111
	v_and_b32_e32 v111, 0xffff0000, v111
	v_mul_f32_e32 v114, v147, v116
	v_mul_f32_e32 v111, v147, v111
	v_cvt_pk_fp8_f32 v110, v114, v111 op_sel:[0,0,1]
	v_lshlrev_b32_e32 v111, 16, v112
	v_mul_f32_e32 v114, v147, v111
	v_and_b32_e32 v111, 0xffff0000, v112
	v_mul_f32_e32 v112, v147, v111
	v_cvt_pk_fp8_f32 v111, v114, v112
	v_lshlrev_b32_e32 v115, 16, v113
	v_and_b32_e32 v113, 0xffff0000, v113
	v_mul_f32_e32 v112, v147, v115
	v_mul_f32_e32 v113, v147, v113
	v_cvt_pk_fp8_f32 v111, v112, v113 op_sel:[0,0,1]
	global_store_dwordx2 v[126:127], v[110:111], off offset:128
	s_nop 0
	v_lshlrev_b32_e32 v110, 16, v106
	v_and_b32_e32 v106, 0xffff0000, v106
	v_mul_f32_e32 v110, v147, v110
	v_mul_f32_e32 v111, v147, v106
	v_cvt_pk_fp8_f32 v106, v110, v111
	v_lshlrev_b32_e32 v112, 16, v107
	v_and_b32_e32 v107, 0xffff0000, v107
	v_mul_f32_e32 v110, v147, v112
	v_mul_f32_e32 v107, v147, v107
	v_cvt_pk_fp8_f32 v106, v110, v107 op_sel:[0,0,1]
	v_lshlrev_b32_e32 v107, 16, v108
	v_mul_f32_e32 v110, v147, v107
	v_and_b32_e32 v107, 0xffff0000, v108
	v_mul_f32_e32 v108, v147, v107
	v_cvt_pk_fp8_f32 v107, v110, v108
	v_lshlrev_b32_e32 v111, 16, v109
	v_and_b32_e32 v109, 0xffff0000, v109
	v_mul_f32_e32 v108, v147, v111
	v_mul_f32_e32 v109, v147, v109
	v_cvt_pk_fp8_f32 v107, v108, v109 op_sel:[0,0,1]
	global_store_dwordx2 v[126:127], v[106:107], off offset:160
	s_nop 0
	v_lshlrev_b32_e32 v106, 16, v102
	v_and_b32_e32 v102, 0xffff0000, v102
	v_mul_f32_e32 v106, v147, v106
	v_mul_f32_e32 v107, v147, v102
	v_cvt_pk_fp8_f32 v102, v106, v107
	v_lshlrev_b32_e32 v108, 16, v103
	v_and_b32_e32 v103, 0xffff0000, v103
	v_mul_f32_e32 v106, v147, v108
	v_mul_f32_e32 v103, v147, v103
	v_cvt_pk_fp8_f32 v102, v106, v103 op_sel:[0,0,1]
	v_lshlrev_b32_e32 v103, 16, v104
	v_mul_f32_e32 v106, v147, v103
	v_and_b32_e32 v103, 0xffff0000, v104
	v_mul_f32_e32 v104, v147, v103
	v_cvt_pk_fp8_f32 v103, v106, v104
	v_lshlrev_b32_e32 v107, 16, v105
	v_and_b32_e32 v105, 0xffff0000, v105
	v_mul_f32_e32 v104, v147, v107
	v_mul_f32_e32 v105, v147, v105
	v_cvt_pk_fp8_f32 v103, v104, v105 op_sel:[0,0,1]
	global_store_dwordx2 v[126:127], v[102:103], off offset:192
	s_nop 0
	v_lshlrev_b32_e32 v102, 16, v98
	v_and_b32_e32 v98, 0xffff0000, v98
	v_mul_f32_e32 v102, v147, v102
	v_mul_f32_e32 v103, v147, v98
	v_cvt_pk_fp8_f32 v98, v102, v103
	v_lshlrev_b32_e32 v104, 16, v99
	v_and_b32_e32 v99, 0xffff0000, v99
	v_mul_f32_e32 v102, v147, v104
	v_mul_f32_e32 v99, v147, v99
	v_cvt_pk_fp8_f32 v98, v102, v99 op_sel:[0,0,1]
	v_lshlrev_b32_e32 v99, 16, v100
	v_mul_f32_e32 v102, v147, v99
	v_and_b32_e32 v99, 0xffff0000, v100
	v_mul_f32_e32 v100, v147, v99
	v_cvt_pk_fp8_f32 v99, v102, v100
	v_lshlrev_b32_e32 v103, 16, v101
	v_and_b32_e32 v101, 0xffff0000, v101
	v_mul_f32_e32 v100, v147, v103
	v_mul_f32_e32 v101, v147, v101
	v_cvt_pk_fp8_f32 v99, v100, v101 op_sel:[0,0,1]
	global_store_dwordx2 v[126:127], v[98:99], off offset:224
	s_nop 0
	v_lshlrev_b32_e32 v98, 16, v94
	v_and_b32_e32 v94, 0xffff0000, v94
	v_mul_f32_e32 v98, v147, v98
	v_mul_f32_e32 v99, v147, v94
	v_cvt_pk_fp8_f32 v94, v98, v99
	v_lshlrev_b32_e32 v100, 16, v95
	v_and_b32_e32 v95, 0xffff0000, v95
	v_mul_f32_e32 v98, v147, v100
	v_mul_f32_e32 v95, v147, v95
	v_cvt_pk_fp8_f32 v94, v98, v95 op_sel:[0,0,1]
	v_lshlrev_b32_e32 v95, 16, v96
	v_mul_f32_e32 v98, v147, v95
	v_and_b32_e32 v95, 0xffff0000, v96
	v_mul_f32_e32 v96, v147, v95
	v_cvt_pk_fp8_f32 v95, v98, v96
	v_lshlrev_b32_e32 v99, 16, v97
	v_and_b32_e32 v97, 0xffff0000, v97
	v_mul_f32_e32 v96, v147, v99
	v_mul_f32_e32 v97, v147, v97
	v_cvt_pk_fp8_f32 v95, v96, v97 op_sel:[0,0,1]
	global_store_dwordx2 v[126:127], v[94:95], off offset:256
	s_nop 0
	v_lshlrev_b32_e32 v94, 16, v90
	v_and_b32_e32 v90, 0xffff0000, v90
	v_mul_f32_e32 v94, v147, v94
	v_mul_f32_e32 v95, v147, v90
	v_cvt_pk_fp8_f32 v90, v94, v95
	v_lshlrev_b32_e32 v96, 16, v91
	v_and_b32_e32 v91, 0xffff0000, v91
	v_mul_f32_e32 v94, v147, v96
	v_mul_f32_e32 v91, v147, v91
	v_cvt_pk_fp8_f32 v90, v94, v91 op_sel:[0,0,1]
	v_lshlrev_b32_e32 v91, 16, v92
	v_mul_f32_e32 v94, v147, v91
	v_and_b32_e32 v91, 0xffff0000, v92
	v_mul_f32_e32 v92, v147, v91
	v_cvt_pk_fp8_f32 v91, v94, v92
	v_lshlrev_b32_e32 v95, 16, v93
	v_and_b32_e32 v93, 0xffff0000, v93
	v_mul_f32_e32 v92, v147, v95
	v_mul_f32_e32 v93, v147, v93
	v_cvt_pk_fp8_f32 v91, v92, v93 op_sel:[0,0,1]
	global_store_dwordx2 v[126:127], v[90:91], off offset:288
	s_nop 0
	v_lshlrev_b32_e32 v90, 16, v86
	v_and_b32_e32 v86, 0xffff0000, v86
	v_mul_f32_e32 v90, v147, v90
	v_mul_f32_e32 v91, v147, v86
	v_cvt_pk_fp8_f32 v86, v90, v91
	v_lshlrev_b32_e32 v92, 16, v87
	v_and_b32_e32 v87, 0xffff0000, v87
	v_mul_f32_e32 v90, v147, v92
	v_mul_f32_e32 v87, v147, v87
	v_cvt_pk_fp8_f32 v86, v90, v87 op_sel:[0,0,1]
	v_lshlrev_b32_e32 v87, 16, v88
	v_mul_f32_e32 v90, v147, v87
	v_and_b32_e32 v87, 0xffff0000, v88
	v_mul_f32_e32 v88, v147, v87
	v_cvt_pk_fp8_f32 v87, v90, v88
	v_lshlrev_b32_e32 v91, 16, v89
	v_and_b32_e32 v89, 0xffff0000, v89
	v_mul_f32_e32 v88, v147, v91
	v_mul_f32_e32 v89, v147, v89
	v_cvt_pk_fp8_f32 v87, v88, v89 op_sel:[0,0,1]
	global_store_dwordx2 v[126:127], v[86:87], off offset:320
	s_nop 0
	v_lshlrev_b32_e32 v86, 16, v82
	v_and_b32_e32 v82, 0xffff0000, v82
	v_mul_f32_e32 v86, v147, v86
	v_mul_f32_e32 v87, v147, v82
	v_cvt_pk_fp8_f32 v82, v86, v87
	v_lshlrev_b32_e32 v88, 16, v83
	v_and_b32_e32 v83, 0xffff0000, v83
	v_mul_f32_e32 v86, v147, v88
	v_mul_f32_e32 v83, v147, v83
	v_cvt_pk_fp8_f32 v82, v86, v83 op_sel:[0,0,1]
	v_lshlrev_b32_e32 v83, 16, v84
	v_mul_f32_e32 v86, v147, v83
	v_and_b32_e32 v83, 0xffff0000, v84
	v_mul_f32_e32 v84, v147, v83
	v_cvt_pk_fp8_f32 v83, v86, v84
	v_lshlrev_b32_e32 v87, 16, v85
	v_and_b32_e32 v85, 0xffff0000, v85
	v_mul_f32_e32 v84, v147, v87
	v_mul_f32_e32 v85, v147, v85
	v_cvt_pk_fp8_f32 v83, v84, v85 op_sel:[0,0,1]
	global_store_dwordx2 v[126:127], v[82:83], off offset:352
	s_nop 0
	v_lshlrev_b32_e32 v82, 16, v78
	v_and_b32_e32 v78, 0xffff0000, v78
	v_mul_f32_e32 v82, v147, v82
	v_mul_f32_e32 v83, v147, v78
	v_cvt_pk_fp8_f32 v78, v82, v83
	v_lshlrev_b32_e32 v84, 16, v79
	v_and_b32_e32 v79, 0xffff0000, v79
	v_mul_f32_e32 v82, v147, v84
	v_mul_f32_e32 v79, v147, v79
	v_cvt_pk_fp8_f32 v78, v82, v79 op_sel:[0,0,1]
	v_lshlrev_b32_e32 v79, 16, v80
	v_mul_f32_e32 v82, v147, v79
	v_and_b32_e32 v79, 0xffff0000, v80
	v_mul_f32_e32 v80, v147, v79
	v_cvt_pk_fp8_f32 v79, v82, v80
	v_lshlrev_b32_e32 v83, 16, v81
	v_and_b32_e32 v81, 0xffff0000, v81
	v_mul_f32_e32 v80, v147, v83
	v_mul_f32_e32 v81, v147, v81
	v_cvt_pk_fp8_f32 v79, v80, v81 op_sel:[0,0,1]
	global_store_dwordx2 v[126:127], v[78:79], off offset:384
	s_nop 0
	v_lshlrev_b32_e32 v78, 16, v74
	v_and_b32_e32 v74, 0xffff0000, v74
	v_mul_f32_e32 v78, v147, v78
	v_mul_f32_e32 v79, v147, v74
	v_cvt_pk_fp8_f32 v74, v78, v79
	v_lshlrev_b32_e32 v80, 16, v75
	v_and_b32_e32 v75, 0xffff0000, v75
	v_mul_f32_e32 v78, v147, v80
	v_mul_f32_e32 v75, v147, v75
	v_cvt_pk_fp8_f32 v74, v78, v75 op_sel:[0,0,1]
	v_lshlrev_b32_e32 v75, 16, v76
	v_mul_f32_e32 v78, v147, v75
	v_and_b32_e32 v75, 0xffff0000, v76
	v_mul_f32_e32 v76, v147, v75
	v_cvt_pk_fp8_f32 v75, v78, v76
	v_lshlrev_b32_e32 v79, 16, v77
	v_and_b32_e32 v77, 0xffff0000, v77
	v_mul_f32_e32 v76, v147, v79
	v_mul_f32_e32 v77, v147, v77
	v_cvt_pk_fp8_f32 v75, v76, v77 op_sel:[0,0,1]
	global_store_dwordx2 v[126:127], v[74:75], off offset:416
	s_nop 0
	v_lshlrev_b32_e32 v74, 16, v70
	v_and_b32_e32 v70, 0xffff0000, v70
	v_mul_f32_e32 v74, v147, v74
	v_mul_f32_e32 v75, v147, v70
	v_cvt_pk_fp8_f32 v70, v74, v75
	v_lshlrev_b32_e32 v76, 16, v71
	v_and_b32_e32 v71, 0xffff0000, v71
	v_mul_f32_e32 v74, v147, v76
	v_mul_f32_e32 v71, v147, v71
	v_cvt_pk_fp8_f32 v70, v74, v71 op_sel:[0,0,1]
	v_lshlrev_b32_e32 v71, 16, v72
	v_mul_f32_e32 v74, v147, v71
	v_and_b32_e32 v71, 0xffff0000, v72
	v_mul_f32_e32 v72, v147, v71
	v_cvt_pk_fp8_f32 v71, v74, v72
	v_lshlrev_b32_e32 v75, 16, v73
	v_and_b32_e32 v73, 0xffff0000, v73
	v_mul_f32_e32 v72, v147, v75
	v_mul_f32_e32 v73, v147, v73
	v_cvt_pk_fp8_f32 v71, v72, v73 op_sel:[0,0,1]
	global_store_dwordx2 v[126:127], v[70:71], off offset:448
	s_nop 0
	v_lshlrev_b32_e32 v70, 16, v66
	v_and_b32_e32 v66, 0xffff0000, v66
	v_mul_f32_e32 v70, v147, v70
	v_mul_f32_e32 v71, v147, v66
	v_cvt_pk_fp8_f32 v66, v70, v71
	v_lshlrev_b32_e32 v72, 16, v67
	v_and_b32_e32 v67, 0xffff0000, v67
	v_mul_f32_e32 v70, v147, v72
	v_mul_f32_e32 v67, v147, v67
	v_cvt_pk_fp8_f32 v66, v70, v67 op_sel:[0,0,1]
	v_lshlrev_b32_e32 v67, 16, v68
	v_mul_f32_e32 v70, v147, v67
	v_and_b32_e32 v67, 0xffff0000, v68
	v_mul_f32_e32 v68, v147, v67
	v_cvt_pk_fp8_f32 v67, v70, v68
	v_lshlrev_b32_e32 v71, 16, v69
	v_and_b32_e32 v69, 0xffff0000, v69
	v_mul_f32_e32 v68, v147, v71
	v_mul_f32_e32 v69, v147, v69
	v_cvt_pk_fp8_f32 v67, v68, v69 op_sel:[0,0,1]
	global_store_dwordx2 v[126:127], v[66:67], off offset:480
	s_nop 0
	v_lshlrev_b32_e32 v66, 16, v62
	v_and_b32_e32 v62, 0xffff0000, v62
	v_mul_f32_e32 v66, v147, v66
	v_mul_f32_e32 v67, v147, v62
	v_cvt_pk_fp8_f32 v62, v66, v67
	v_lshlrev_b32_e32 v68, 16, v63
	v_and_b32_e32 v63, 0xffff0000, v63
	v_mul_f32_e32 v66, v147, v68
	v_mul_f32_e32 v63, v147, v63
	v_cvt_pk_fp8_f32 v62, v66, v63 op_sel:[0,0,1]
	v_lshlrev_b32_e32 v63, 16, v64
	v_mul_f32_e32 v66, v147, v63
	v_and_b32_e32 v63, 0xffff0000, v64
	v_mul_f32_e32 v64, v147, v63
	v_cvt_pk_fp8_f32 v63, v66, v64
	v_lshlrev_b32_e32 v67, 16, v65
	v_and_b32_e32 v65, 0xffff0000, v65
	v_mul_f32_e32 v64, v147, v67
	v_mul_f32_e32 v65, v147, v65
	v_cvt_pk_fp8_f32 v63, v64, v65 op_sel:[0,0,1]
	global_store_dwordx2 v[126:127], v[62:63], off offset:512
	s_nop 0
	v_lshlrev_b32_e32 v62, 16, v58
	v_and_b32_e32 v58, 0xffff0000, v58
	v_mul_f32_e32 v62, v147, v62
	v_mul_f32_e32 v63, v147, v58
	v_cvt_pk_fp8_f32 v58, v62, v63
	v_lshlrev_b32_e32 v64, 16, v59
	v_and_b32_e32 v59, 0xffff0000, v59
	v_mul_f32_e32 v62, v147, v64
	v_mul_f32_e32 v59, v147, v59
	v_cvt_pk_fp8_f32 v58, v62, v59 op_sel:[0,0,1]
	v_lshlrev_b32_e32 v59, 16, v60
	v_mul_f32_e32 v62, v147, v59
	v_and_b32_e32 v59, 0xffff0000, v60
	v_mul_f32_e32 v60, v147, v59
	v_cvt_pk_fp8_f32 v59, v62, v60
	v_lshlrev_b32_e32 v63, 16, v61
	v_and_b32_e32 v61, 0xffff0000, v61
	v_mul_f32_e32 v60, v147, v63
	v_mul_f32_e32 v61, v147, v61
	v_cvt_pk_fp8_f32 v59, v60, v61 op_sel:[0,0,1]
	global_store_dwordx2 v[126:127], v[58:59], off offset:544
	s_nop 0
	v_lshlrev_b32_e32 v58, 16, v54
	v_and_b32_e32 v54, 0xffff0000, v54
	v_mul_f32_e32 v58, v147, v58
	v_mul_f32_e32 v59, v147, v54
	v_cvt_pk_fp8_f32 v54, v58, v59
	v_lshlrev_b32_e32 v60, 16, v55
	v_and_b32_e32 v55, 0xffff0000, v55
	v_mul_f32_e32 v58, v147, v60
	v_mul_f32_e32 v55, v147, v55
	v_cvt_pk_fp8_f32 v54, v58, v55 op_sel:[0,0,1]
	v_lshlrev_b32_e32 v55, 16, v56
	v_mul_f32_e32 v58, v147, v55
	v_and_b32_e32 v55, 0xffff0000, v56
	v_mul_f32_e32 v56, v147, v55
	v_cvt_pk_fp8_f32 v55, v58, v56
	v_lshlrev_b32_e32 v59, 16, v57
	v_and_b32_e32 v57, 0xffff0000, v57
	v_mul_f32_e32 v56, v147, v59
	v_mul_f32_e32 v57, v147, v57
	v_cvt_pk_fp8_f32 v55, v56, v57 op_sel:[0,0,1]
	global_store_dwordx2 v[126:127], v[54:55], off offset:576
	s_nop 0
	v_lshlrev_b32_e32 v54, 16, v50
	v_and_b32_e32 v50, 0xffff0000, v50
	v_mul_f32_e32 v54, v147, v54
	v_mul_f32_e32 v55, v147, v50
	v_cvt_pk_fp8_f32 v50, v54, v55
	v_lshlrev_b32_e32 v56, 16, v51
	v_and_b32_e32 v51, 0xffff0000, v51
	v_mul_f32_e32 v54, v147, v56
	v_mul_f32_e32 v51, v147, v51
	v_cvt_pk_fp8_f32 v50, v54, v51 op_sel:[0,0,1]
	v_lshlrev_b32_e32 v51, 16, v52
	v_mul_f32_e32 v54, v147, v51
	v_and_b32_e32 v51, 0xffff0000, v52
	v_mul_f32_e32 v52, v147, v51
	v_cvt_pk_fp8_f32 v51, v54, v52
	v_lshlrev_b32_e32 v55, 16, v53
	v_and_b32_e32 v53, 0xffff0000, v53
	v_mul_f32_e32 v52, v147, v55
	v_mul_f32_e32 v53, v147, v53
	v_cvt_pk_fp8_f32 v51, v52, v53 op_sel:[0,0,1]
	global_store_dwordx2 v[126:127], v[50:51], off offset:608
	s_nop 0
	v_lshlrev_b32_e32 v50, 16, v46
	v_and_b32_e32 v46, 0xffff0000, v46
	v_mul_f32_e32 v50, v147, v50
	v_mul_f32_e32 v51, v147, v46
	v_cvt_pk_fp8_f32 v46, v50, v51
	v_lshlrev_b32_e32 v52, 16, v47
	v_and_b32_e32 v47, 0xffff0000, v47
	v_mul_f32_e32 v50, v147, v52
	v_mul_f32_e32 v47, v147, v47
	v_cvt_pk_fp8_f32 v46, v50, v47 op_sel:[0,0,1]
	v_lshlrev_b32_e32 v47, 16, v48
	v_mul_f32_e32 v50, v147, v47
	v_and_b32_e32 v47, 0xffff0000, v48
	v_mul_f32_e32 v48, v147, v47
	v_cvt_pk_fp8_f32 v47, v50, v48
	v_lshlrev_b32_e32 v51, 16, v49
	v_and_b32_e32 v49, 0xffff0000, v49
	v_mul_f32_e32 v48, v147, v51
	v_mul_f32_e32 v49, v147, v49
	v_cvt_pk_fp8_f32 v47, v48, v49 op_sel:[0,0,1]
	global_store_dwordx2 v[126:127], v[46:47], off offset:640
	s_nop 0
	v_lshlrev_b32_e32 v46, 16, v42
	v_and_b32_e32 v42, 0xffff0000, v42
	v_mul_f32_e32 v46, v147, v46
	v_mul_f32_e32 v47, v147, v42
	v_cvt_pk_fp8_f32 v42, v46, v47
	v_lshlrev_b32_e32 v48, 16, v43
	v_and_b32_e32 v43, 0xffff0000, v43
	v_mul_f32_e32 v46, v147, v48
	v_mul_f32_e32 v43, v147, v43
	v_cvt_pk_fp8_f32 v42, v46, v43 op_sel:[0,0,1]
	v_lshlrev_b32_e32 v43, 16, v44
	v_mul_f32_e32 v46, v147, v43
	v_and_b32_e32 v43, 0xffff0000, v44
	v_mul_f32_e32 v44, v147, v43
	v_cvt_pk_fp8_f32 v43, v46, v44
	v_lshlrev_b32_e32 v47, 16, v45
	v_and_b32_e32 v45, 0xffff0000, v45
	v_mul_f32_e32 v44, v147, v47
	v_mul_f32_e32 v45, v147, v45
	v_cvt_pk_fp8_f32 v43, v44, v45 op_sel:[0,0,1]
	global_store_dwordx2 v[126:127], v[42:43], off offset:672
	s_nop 0
	v_lshlrev_b32_e32 v42, 16, v38
	v_and_b32_e32 v38, 0xffff0000, v38
	v_mul_f32_e32 v42, v147, v42
	v_mul_f32_e32 v43, v147, v38
	v_cvt_pk_fp8_f32 v38, v42, v43
	v_lshlrev_b32_e32 v44, 16, v39
	v_and_b32_e32 v39, 0xffff0000, v39
	v_mul_f32_e32 v42, v147, v44
	v_mul_f32_e32 v39, v147, v39
	v_cvt_pk_fp8_f32 v38, v42, v39 op_sel:[0,0,1]
	v_lshlrev_b32_e32 v39, 16, v40
	v_mul_f32_e32 v42, v147, v39
	v_and_b32_e32 v39, 0xffff0000, v40
	v_mul_f32_e32 v40, v147, v39
	v_cvt_pk_fp8_f32 v39, v42, v40
	v_lshlrev_b32_e32 v43, 16, v41
	v_and_b32_e32 v41, 0xffff0000, v41
	v_mul_f32_e32 v40, v147, v43
	v_mul_f32_e32 v41, v147, v41
	v_cvt_pk_fp8_f32 v39, v40, v41 op_sel:[0,0,1]
	global_store_dwordx2 v[126:127], v[38:39], off offset:704
	s_nop 0
	v_lshlrev_b32_e32 v38, 16, v34
	v_and_b32_e32 v34, 0xffff0000, v34
	v_mul_f32_e32 v38, v147, v38
	v_mul_f32_e32 v39, v147, v34
	v_cvt_pk_fp8_f32 v34, v38, v39
	v_lshlrev_b32_e32 v40, 16, v35
	v_and_b32_e32 v35, 0xffff0000, v35
	v_mul_f32_e32 v38, v147, v40
	v_mul_f32_e32 v35, v147, v35
	v_cvt_pk_fp8_f32 v34, v38, v35 op_sel:[0,0,1]
	v_lshlrev_b32_e32 v35, 16, v36
	v_mul_f32_e32 v38, v147, v35
	v_and_b32_e32 v35, 0xffff0000, v36
	v_mul_f32_e32 v36, v147, v35
	v_cvt_pk_fp8_f32 v35, v38, v36
	v_lshlrev_b32_e32 v39, 16, v37
	v_and_b32_e32 v37, 0xffff0000, v37
	v_mul_f32_e32 v36, v147, v39
	v_mul_f32_e32 v37, v147, v37
	v_cvt_pk_fp8_f32 v35, v36, v37 op_sel:[0,0,1]
	global_store_dwordx2 v[126:127], v[34:35], off offset:736
	s_nop 0
	v_lshlrev_b32_e32 v34, 16, v30
	v_and_b32_e32 v30, 0xffff0000, v30
	v_mul_f32_e32 v34, v147, v34
	v_mul_f32_e32 v35, v147, v30
	v_cvt_pk_fp8_f32 v30, v34, v35
	v_lshlrev_b32_e32 v36, 16, v31
	v_and_b32_e32 v31, 0xffff0000, v31
	v_mul_f32_e32 v34, v147, v36
	v_mul_f32_e32 v31, v147, v31
	v_cvt_pk_fp8_f32 v30, v34, v31 op_sel:[0,0,1]
	v_lshlrev_b32_e32 v31, 16, v32
	v_mul_f32_e32 v34, v147, v31
	v_and_b32_e32 v31, 0xffff0000, v32
	v_mul_f32_e32 v32, v147, v31
	v_cvt_pk_fp8_f32 v31, v34, v32
	v_lshlrev_b32_e32 v35, 16, v33
	v_and_b32_e32 v33, 0xffff0000, v33
	v_mul_f32_e32 v32, v147, v35
	v_mul_f32_e32 v33, v147, v33
	v_cvt_pk_fp8_f32 v31, v32, v33 op_sel:[0,0,1]
	global_store_dwordx2 v[126:127], v[30:31], off offset:768
	s_nop 0
	v_lshlrev_b32_e32 v30, 16, v26
	v_and_b32_e32 v26, 0xffff0000, v26
	v_mul_f32_e32 v30, v147, v30
	v_mul_f32_e32 v31, v147, v26
	v_cvt_pk_fp8_f32 v26, v30, v31
	v_lshlrev_b32_e32 v32, 16, v27
	v_and_b32_e32 v27, 0xffff0000, v27
	v_mul_f32_e32 v30, v147, v32
	v_mul_f32_e32 v27, v147, v27
	v_cvt_pk_fp8_f32 v26, v30, v27 op_sel:[0,0,1]
	v_lshlrev_b32_e32 v27, 16, v28
	v_mul_f32_e32 v30, v147, v27
	v_and_b32_e32 v27, 0xffff0000, v28
	v_mul_f32_e32 v28, v147, v27
	v_cvt_pk_fp8_f32 v27, v30, v28
	v_lshlrev_b32_e32 v31, 16, v29
	v_and_b32_e32 v29, 0xffff0000, v29
	v_mul_f32_e32 v28, v147, v31
	v_mul_f32_e32 v29, v147, v29
	v_cvt_pk_fp8_f32 v27, v28, v29 op_sel:[0,0,1]
	global_store_dwordx2 v[126:127], v[26:27], off offset:800
	s_nop 0
	v_lshlrev_b32_e32 v26, 16, v22
	v_and_b32_e32 v22, 0xffff0000, v22
	v_mul_f32_e32 v26, v147, v26
	v_mul_f32_e32 v27, v147, v22
	v_cvt_pk_fp8_f32 v22, v26, v27
	v_lshlrev_b32_e32 v28, 16, v23
	v_and_b32_e32 v23, 0xffff0000, v23
	v_mul_f32_e32 v26, v147, v28
	v_mul_f32_e32 v23, v147, v23
	v_cvt_pk_fp8_f32 v22, v26, v23 op_sel:[0,0,1]
	v_lshlrev_b32_e32 v23, 16, v24
	v_mul_f32_e32 v26, v147, v23
	v_and_b32_e32 v23, 0xffff0000, v24
	v_mul_f32_e32 v24, v147, v23
	v_cvt_pk_fp8_f32 v23, v26, v24
	v_lshlrev_b32_e32 v27, 16, v25
	v_and_b32_e32 v25, 0xffff0000, v25
	v_mul_f32_e32 v24, v147, v27
	v_mul_f32_e32 v25, v147, v25
	v_cvt_pk_fp8_f32 v23, v24, v25 op_sel:[0,0,1]
	global_store_dwordx2 v[126:127], v[22:23], off offset:832
	s_nop 0
	v_lshlrev_b32_e32 v22, 16, v18
	v_and_b32_e32 v18, 0xffff0000, v18
	v_mul_f32_e32 v22, v147, v22
	v_mul_f32_e32 v23, v147, v18
	v_cvt_pk_fp8_f32 v18, v22, v23
	v_lshlrev_b32_e32 v24, 16, v19
	v_and_b32_e32 v19, 0xffff0000, v19
	v_mul_f32_e32 v22, v147, v24
	v_mul_f32_e32 v19, v147, v19
	v_cvt_pk_fp8_f32 v18, v22, v19 op_sel:[0,0,1]
	v_lshlrev_b32_e32 v19, 16, v20
	v_mul_f32_e32 v22, v147, v19
	v_and_b32_e32 v19, 0xffff0000, v20
	v_mul_f32_e32 v20, v147, v19
	v_cvt_pk_fp8_f32 v19, v22, v20
	v_lshlrev_b32_e32 v23, 16, v21
	v_and_b32_e32 v21, 0xffff0000, v21
	v_mul_f32_e32 v20, v147, v23
	v_mul_f32_e32 v21, v147, v21
	v_cvt_pk_fp8_f32 v19, v20, v21 op_sel:[0,0,1]
	global_store_dwordx2 v[126:127], v[18:19], off offset:864
	s_nop 0
	v_lshlrev_b32_e32 v18, 16, v14
	v_and_b32_e32 v14, 0xffff0000, v14
	v_mul_f32_e32 v18, v147, v18
	v_mul_f32_e32 v19, v147, v14
	v_cvt_pk_fp8_f32 v14, v18, v19
	v_lshlrev_b32_e32 v20, 16, v15
	v_and_b32_e32 v15, 0xffff0000, v15
	v_mul_f32_e32 v18, v147, v20
	v_mul_f32_e32 v15, v147, v15
	v_cvt_pk_fp8_f32 v14, v18, v15 op_sel:[0,0,1]
	v_lshlrev_b32_e32 v15, 16, v16
	v_mul_f32_e32 v18, v147, v15
	v_and_b32_e32 v15, 0xffff0000, v16
	v_mul_f32_e32 v16, v147, v15
	v_cvt_pk_fp8_f32 v15, v18, v16
	v_lshlrev_b32_e32 v19, 16, v17
	v_and_b32_e32 v17, 0xffff0000, v17
	v_mul_f32_e32 v16, v147, v19
	v_mul_f32_e32 v17, v147, v17
	v_cvt_pk_fp8_f32 v15, v16, v17 op_sel:[0,0,1]
	global_store_dwordx2 v[126:127], v[14:15], off offset:896
	s_nop 0
	v_lshlrev_b32_e32 v14, 16, v10
	v_and_b32_e32 v10, 0xffff0000, v10
	v_mul_f32_e32 v14, v147, v14
	v_mul_f32_e32 v15, v147, v10
	v_cvt_pk_fp8_f32 v10, v14, v15
	v_lshlrev_b32_e32 v16, 16, v11
	v_and_b32_e32 v11, 0xffff0000, v11
	v_mul_f32_e32 v14, v147, v16
	v_mul_f32_e32 v11, v147, v11
	v_cvt_pk_fp8_f32 v10, v14, v11 op_sel:[0,0,1]
	v_lshlrev_b32_e32 v11, 16, v12
	v_mul_f32_e32 v14, v147, v11
	v_and_b32_e32 v11, 0xffff0000, v12
	v_mul_f32_e32 v12, v147, v11
	v_cvt_pk_fp8_f32 v11, v14, v12
	v_lshlrev_b32_e32 v15, 16, v13
	v_and_b32_e32 v13, 0xffff0000, v13
	v_mul_f32_e32 v12, v147, v15
	v_mul_f32_e32 v13, v147, v13
	v_cvt_pk_fp8_f32 v11, v12, v13 op_sel:[0,0,1]
	global_store_dwordx2 v[126:127], v[10:11], off offset:928
	s_nop 0
	v_lshlrev_b32_e32 v10, 16, v6
	v_and_b32_e32 v6, 0xffff0000, v6
	v_mul_f32_e32 v10, v147, v10
	v_mul_f32_e32 v11, v147, v6
	v_cvt_pk_fp8_f32 v6, v10, v11
	v_lshlrev_b32_e32 v12, 16, v7
	v_and_b32_e32 v7, 0xffff0000, v7
	v_mul_f32_e32 v10, v147, v12
	v_mul_f32_e32 v7, v147, v7
	v_cvt_pk_fp8_f32 v6, v10, v7 op_sel:[0,0,1]
	v_lshlrev_b32_e32 v7, 16, v8
	v_mul_f32_e32 v10, v147, v7
	v_and_b32_e32 v7, 0xffff0000, v8
	v_mul_f32_e32 v8, v147, v7
	v_cvt_pk_fp8_f32 v7, v10, v8
	v_lshlrev_b32_e32 v11, 16, v9
	v_and_b32_e32 v9, 0xffff0000, v9
	v_mul_f32_e32 v8, v147, v11
	v_mul_f32_e32 v9, v147, v9
	v_cvt_pk_fp8_f32 v7, v8, v9 op_sel:[0,0,1]
	global_store_dwordx2 v[126:127], v[6:7], off offset:960
	s_nop 0
	v_lshlrev_b32_e32 v6, 16, v2
	v_and_b32_e32 v2, 0xffff0000, v2
	v_mul_f32_e32 v6, v147, v6
	v_mul_f32_e32 v7, v147, v2
	v_cvt_pk_fp8_f32 v2, v6, v7
	v_lshlrev_b32_e32 v8, 16, v3
	v_and_b32_e32 v3, 0xffff0000, v3
	v_mul_f32_e32 v6, v147, v8
	v_mul_f32_e32 v3, v147, v3
	v_cvt_pk_fp8_f32 v2, v6, v3 op_sel:[0,0,1]
	v_lshlrev_b32_e32 v3, 16, v4
	v_mul_f32_e32 v6, v147, v3
	v_and_b32_e32 v3, 0xffff0000, v4
	v_mul_f32_e32 v4, v147, v3
	v_cvt_pk_fp8_f32 v3, v6, v4
	v_lshlrev_b32_e32 v7, 16, v5
	v_and_b32_e32 v5, 0xffff0000, v5
	v_mul_f32_e32 v4, v147, v7
	v_mul_f32_e32 v5, v147, v5
	v_cvt_pk_fp8_f32 v3, v4, v5 op_sel:[0,0,1]
	ds_bpermute_b32 v4, v179, v145
	ds_bpermute_b32 v5, v185, v145
	global_store_dwordx2 v[126:127], v[2:3], off offset:992
	ds_bpermute_b32 v2, v181, v145
	s_waitcnt lgkmcnt(2)
	v_fma_f32 v3, v130, v4, v172
	v_fma_f32 v4, v134, v4, v173
	s_waitcnt lgkmcnt(0)
	ds_write2_b32 v180, v3, v4 offset1:16
	ds_bpermute_b32 v3, v183, v145
	s_waitcnt lgkmcnt(2)
	v_fma_f32 v4, v131, v2, v172
	v_fma_f32 v2, v135, v2, v173
	ds_write2_b32 v182, v4, v2 offset1:16
	s_waitcnt lgkmcnt(1)
	v_fma_f32 v2, v132, v3, v172
	v_fma_f32 v3, v136, v3, v173
	ds_write2_b32 v184, v2, v3 offset1:16
	v_fma_f32 v2, v133, v5, v172
	v_fma_f32 v3, v137, v5, v173
	ds_write2_b32 v186, v2, v3 offset1:16
	s_waitcnt lgkmcnt(0)
	s_and_saveexec_b64 s[20:21], s[6:7]
	s_cbranch_execz .LBB0_437
	v_add_u32_e32 v2, s0, v176
	ds_read2_b32 v[32:33], v2 offset1:1
	ds_read2_b32 v[30:31], v2 offset0:2 offset1:3
	ds_read2_b32 v[28:29], v2 offset0:4 offset1:5
	ds_read2_b32 v[26:27], v2 offset0:6 offset1:7
	ds_read2_b32 v[24:25], v2 offset0:8 offset1:9
	ds_read2_b32 v[22:23], v2 offset0:10 offset1:11
	ds_read2_b32 v[20:21], v2 offset0:12 offset1:13
	ds_read2_b32 v[18:19], v2 offset0:14 offset1:15
	ds_read2_b32 v[16:17], v2 offset0:16 offset1:17
	ds_read2_b32 v[14:15], v2 offset0:18 offset1:19
	ds_read2_b32 v[12:13], v2 offset0:20 offset1:21
	ds_read2_b32 v[10:11], v2 offset0:22 offset1:23
	ds_read2_b32 v[8:9], v2 offset0:24 offset1:25
	ds_read2_b32 v[6:7], v2 offset0:26 offset1:27
	ds_read2_b32 v[4:5], v2 offset0:28 offset1:29
	ds_read2_b32 v[2:3], v2 offset0:30 offset1:31
	s_waitcnt lgkmcnt(14)
	v_cmp_gt_f32_e32 vcc, v33, v32
	s_nop 1
	v_cndmask_b32_e32 v35, v32, v33, vcc
	v_cndmask_b32_e64 v34, 0, 1, vcc
	v_cmp_gt_f32_e32 vcc, v30, v35
	s_nop 1
	v_cndmask_b32_e32 v35, v35, v30, vcc
	v_cndmask_b32_e64 v34, v34, 2, vcc
	v_cmp_gt_f32_e32 vcc, v31, v35
	s_nop 1
	v_cndmask_b32_e32 v35, v35, v31, vcc
	v_cndmask_b32_e64 v34, v34, 3, vcc
	s_waitcnt lgkmcnt(13)
	v_cmp_gt_f32_e32 vcc, v28, v35
	s_nop 1
	v_cndmask_b32_e32 v35, v35, v28, vcc
	v_cndmask_b32_e64 v34, v34, 4, vcc
	v_cmp_gt_f32_e32 vcc, v29, v35
	s_nop 1
	v_cndmask_b32_e32 v35, v35, v29, vcc
	v_cndmask_b32_e64 v34, v34, 5, vcc
	s_waitcnt lgkmcnt(12)
	v_cmp_gt_f32_e32 vcc, v26, v35
	s_nop 1
	v_cndmask_b32_e32 v35, v35, v26, vcc
	v_cndmask_b32_e64 v34, v34, 6, vcc
	v_cmp_gt_f32_e32 vcc, v27, v35
	s_nop 1
	v_cndmask_b32_e32 v35, v35, v27, vcc
	v_cndmask_b32_e64 v34, v34, 7, vcc
	s_waitcnt lgkmcnt(11)
	v_cmp_gt_f32_e32 vcc, v24, v35
	s_nop 1
	v_cndmask_b32_e32 v35, v35, v24, vcc
	v_cndmask_b32_e64 v34, v34, 8, vcc
	v_cmp_gt_f32_e32 vcc, v25, v35
	s_nop 1
	v_cndmask_b32_e32 v35, v35, v25, vcc
	v_cndmask_b32_e64 v34, v34, 9, vcc
	s_waitcnt lgkmcnt(10)
	v_cmp_gt_f32_e32 vcc, v22, v35
	s_nop 1
	v_cndmask_b32_e32 v35, v35, v22, vcc
	v_cndmask_b32_e64 v34, v34, 10, vcc
	v_cmp_gt_f32_e32 vcc, v23, v35
	s_nop 1
	v_cndmask_b32_e32 v35, v35, v23, vcc
	v_cndmask_b32_e64 v34, v34, 11, vcc
	s_waitcnt lgkmcnt(9)
	v_cmp_gt_f32_e32 vcc, v20, v35
	s_nop 1
	v_cndmask_b32_e32 v35, v35, v20, vcc
	v_cndmask_b32_e64 v34, v34, 12, vcc
	v_cmp_gt_f32_e32 vcc, v21, v35
	s_nop 1
	v_cndmask_b32_e32 v35, v35, v21, vcc
	v_cndmask_b32_e64 v34, v34, 13, vcc
	s_waitcnt lgkmcnt(8)
	v_cmp_gt_f32_e32 vcc, v18, v35
	s_nop 1
	v_cndmask_b32_e32 v35, v35, v18, vcc
	v_cndmask_b32_e64 v34, v34, 14, vcc
	v_cmp_gt_f32_e32 vcc, v19, v35
	s_nop 1
	v_cndmask_b32_e32 v35, v35, v19, vcc
	v_cndmask_b32_e64 v34, v34, 15, vcc
	s_waitcnt lgkmcnt(7)
	v_cmp_gt_f32_e32 vcc, v16, v35
	s_nop 1
	v_cndmask_b32_e32 v35, v35, v16, vcc
	v_cndmask_b32_e64 v34, v34, 16, vcc
	v_cmp_gt_f32_e32 vcc, v17, v35
	s_nop 1
	v_cndmask_b32_e32 v35, v35, v17, vcc
	v_cndmask_b32_e64 v34, v34, 17, vcc
	s_waitcnt lgkmcnt(6)
	v_cmp_gt_f32_e32 vcc, v14, v35
	s_nop 1
	v_cndmask_b32_e32 v35, v35, v14, vcc
	v_cndmask_b32_e64 v34, v34, 18, vcc
	v_cmp_gt_f32_e32 vcc, v15, v35
	s_nop 1
	v_cndmask_b32_e32 v35, v35, v15, vcc
	v_cndmask_b32_e64 v34, v34, 19, vcc
	s_waitcnt lgkmcnt(5)
	v_cmp_gt_f32_e32 vcc, v12, v35
	s_nop 1
	v_cndmask_b32_e32 v35, v35, v12, vcc
	v_cndmask_b32_e64 v34, v34, 20, vcc
	v_cmp_gt_f32_e32 vcc, v13, v35
	s_nop 1
	v_cndmask_b32_e32 v35, v35, v13, vcc
	v_cndmask_b32_e64 v34, v34, 21, vcc
	s_waitcnt lgkmcnt(4)
	v_cmp_gt_f32_e32 vcc, v10, v35
	s_nop 1
	v_cndmask_b32_e32 v35, v35, v10, vcc
	v_cndmask_b32_e64 v34, v34, 22, vcc
	v_cmp_gt_f32_e32 vcc, v11, v35
	s_nop 1
	v_cndmask_b32_e32 v35, v35, v11, vcc
	v_cndmask_b32_e64 v34, v34, 23, vcc
	s_waitcnt lgkmcnt(3)
	v_cmp_gt_f32_e32 vcc, v8, v35
	s_nop 1
	v_cndmask_b32_e32 v35, v35, v8, vcc
	v_cndmask_b32_e64 v34, v34, 24, vcc
	v_cmp_gt_f32_e32 vcc, v9, v35
	s_nop 1
	v_cndmask_b32_e32 v35, v35, v9, vcc
	v_cndmask_b32_e64 v34, v34, 25, vcc
	s_waitcnt lgkmcnt(2)
	v_cmp_gt_f32_e32 vcc, v6, v35
	s_nop 1
	v_cndmask_b32_e32 v35, v35, v6, vcc
	v_cndmask_b32_e64 v34, v34, 26, vcc
	v_cmp_gt_f32_e32 vcc, v7, v35
	s_nop 1
	v_cndmask_b32_e32 v35, v35, v7, vcc
	v_cndmask_b32_e64 v34, v34, 27, vcc
	s_waitcnt lgkmcnt(1)
	v_cmp_gt_f32_e32 vcc, v4, v35
	s_nop 1
	v_cndmask_b32_e32 v35, v35, v4, vcc
	v_cndmask_b32_e64 v34, v34, 28, vcc
	v_cmp_gt_f32_e32 vcc, v5, v35
	s_nop 1
	v_cndmask_b32_e32 v35, v35, v5, vcc
	v_cndmask_b32_e64 v34, v34, 29, vcc
	s_waitcnt lgkmcnt(0)
	v_cmp_gt_f32_e32 vcc, v2, v35
	s_nop 1
	v_cndmask_b32_e32 v35, v35, v2, vcc
	v_cndmask_b32_e64 v34, v34, 30, vcc
	v_cmp_gt_f32_e32 vcc, v3, v35
	s_nop 1
	v_cndmask_b32_e64 v146, v34, 31, vcc
	v_cndmask_b32_e32 v34, v35, v3, vcc
	v_cmp_eq_u32_e32 vcc, 0, v146
	v_lshlrev_b32_e64 v36, v146, 1
	v_and_b32_e32 v38, 2, v36
	v_cndmask_b32_e32 v37, v32, v198, vcc
	v_cmp_gt_f32_e64 s[8:9], v33, v37
	v_cndmask_b32_e64 v35, 0, -1, vcc
	s_or_b64 vcc, vcc, s[8:9]
	v_cndmask_b32_e64 v39, 0, 1, vcc
	v_cndmask_b32_e32 v40, v32, v33, vcc
	v_cmp_eq_u32_e32 vcc, 0, v38
	v_and_b32_e32 v38, 4, v36
	s_nop 0
	v_cndmask_b32_e32 v37, v37, v40, vcc
	v_cndmask_b32_e32 v35, v35, v39, vcc
	v_cmp_eq_u32_e32 vcc, 0, v38
	v_cmp_gt_f32_e64 s[8:9], v30, v37
	s_and_b64 vcc, vcc, s[8:9]
	v_cndmask_b32_e64 v35, v35, 2, vcc
	v_cndmask_b32_e32 v37, v37, v30, vcc
	v_and_b32_e32 v38, 8, v36
	v_cmp_gt_i32_e64 s[8:9], 0, v35
	v_cmp_gt_f32_e64 s[10:11], v31, v37
	v_cmp_eq_u32_e32 vcc, 0, v38
	s_or_b64 s[8:9], s[8:9], s[10:11]
	s_and_b64 vcc, vcc, s[8:9]
	v_cndmask_b32_e64 v35, v35, 3, vcc
	v_cndmask_b32_e32 v37, v37, v31, vcc
	v_and_b32_e32 v38, 16, v36
	v_cmp_gt_i32_e64 s[8:9], 0, v35
	v_cmp_gt_f32_e64 s[10:11], v28, v37
	v_cmp_eq_u32_e32 vcc, 0, v38
	s_or_b64 s[8:9], s[8:9], s[10:11]
	s_and_b64 vcc, vcc, s[8:9]
	v_cndmask_b32_e64 v35, v35, 4, vcc
	v_cndmask_b32_e32 v37, v37, v28, vcc
	v_and_b32_e32 v38, 32, v36
	v_cmp_gt_i32_e64 s[8:9], 0, v35
	v_cmp_gt_f32_e64 s[10:11], v29, v37
	v_cmp_eq_u32_e32 vcc, 0, v38
	s_or_b64 s[8:9], s[8:9], s[10:11]
	s_and_b64 vcc, vcc, s[8:9]
	v_cndmask_b32_e64 v35, v35, 5, vcc
	v_cndmask_b32_e32 v37, v37, v29, vcc
	v_and_b32_e32 v38, 64, v36
	v_cmp_gt_i32_e64 s[8:9], 0, v35
	v_cmp_gt_f32_e64 s[10:11], v26, v37
	v_cmp_eq_u32_e32 vcc, 0, v38
	s_or_b64 s[8:9], s[8:9], s[10:11]
	s_and_b64 vcc, vcc, s[8:9]
	v_cndmask_b32_e64 v35, v35, 6, vcc
	v_cndmask_b32_e32 v37, v37, v26, vcc
	v_and_b32_e32 v38, 0x80, v36
	v_cmp_gt_i32_e64 s[8:9], 0, v35
	v_cmp_gt_f32_e64 s[10:11], v27, v37
	v_cmp_eq_u32_e32 vcc, 0, v38
	s_or_b64 s[8:9], s[8:9], s[10:11]
	s_and_b64 vcc, vcc, s[8:9]
	v_cndmask_b32_e64 v35, v35, 7, vcc
	v_cndmask_b32_e32 v37, v37, v27, vcc
	v_and_b32_e32 v38, 0x100, v36
	v_cmp_gt_i32_e64 s[8:9], 0, v35
	v_cmp_gt_f32_e64 s[10:11], v24, v37
	v_cmp_eq_u32_e32 vcc, 0, v38
	s_or_b64 s[8:9], s[8:9], s[10:11]
	s_and_b64 vcc, vcc, s[8:9]
	v_cndmask_b32_e64 v35, v35, 8, vcc
	v_cndmask_b32_e32 v37, v37, v24, vcc
	v_and_b32_e32 v38, 0x200, v36
	v_cmp_gt_i32_e64 s[8:9], 0, v35
	v_cmp_gt_f32_e64 s[10:11], v25, v37
	v_cmp_eq_u32_e32 vcc, 0, v38
	s_or_b64 s[8:9], s[8:9], s[10:11]
	s_and_b64 vcc, vcc, s[8:9]
	v_cndmask_b32_e64 v35, v35, 9, vcc
	v_cndmask_b32_e32 v37, v37, v25, vcc
	v_and_b32_e32 v38, 0x400, v36
	v_cmp_gt_i32_e64 s[8:9], 0, v35
	v_cmp_gt_f32_e64 s[10:11], v22, v37
	v_cmp_eq_u32_e32 vcc, 0, v38
	s_or_b64 s[8:9], s[8:9], s[10:11]
	s_and_b64 vcc, vcc, s[8:9]
	v_cndmask_b32_e64 v35, v35, 10, vcc
	v_cndmask_b32_e32 v37, v37, v22, vcc
	v_and_b32_e32 v38, 0x800, v36
	v_cmp_gt_i32_e64 s[8:9], 0, v35
	v_cmp_gt_f32_e64 s[10:11], v23, v37
	v_cmp_eq_u32_e32 vcc, 0, v38
	s_or_b64 s[8:9], s[8:9], s[10:11]
	s_and_b64 vcc, vcc, s[8:9]
	v_cndmask_b32_e64 v35, v35, 11, vcc
	v_cndmask_b32_e32 v37, v37, v23, vcc
	v_and_b32_e32 v38, 0x1000, v36
	v_cmp_gt_i32_e64 s[8:9], 0, v35
	v_cmp_gt_f32_e64 s[10:11], v20, v37
	v_cmp_eq_u32_e32 vcc, 0, v38
	s_or_b64 s[8:9], s[8:9], s[10:11]
	s_and_b64 vcc, vcc, s[8:9]
	v_cndmask_b32_e64 v35, v35, 12, vcc
	v_cndmask_b32_e32 v37, v37, v20, vcc
	v_and_b32_e32 v38, 0x2000, v36
	v_cmp_gt_i32_e64 s[8:9], 0, v35
	v_cmp_gt_f32_e64 s[10:11], v21, v37
	v_cmp_eq_u32_e32 vcc, 0, v38
	s_or_b64 s[8:9], s[8:9], s[10:11]
	s_and_b64 vcc, vcc, s[8:9]
	v_cndmask_b32_e64 v35, v35, 13, vcc
	v_cndmask_b32_e32 v37, v37, v21, vcc
	v_and_b32_e32 v38, 0x4000, v36
	v_cmp_gt_i32_e64 s[8:9], 0, v35
	v_cmp_gt_f32_e64 s[10:11], v18, v37
	v_cmp_eq_u32_e32 vcc, 0, v38
	s_or_b64 s[8:9], s[8:9], s[10:11]
	s_and_b64 vcc, vcc, s[8:9]
	v_cndmask_b32_e64 v35, v35, 14, vcc
	v_cndmask_b32_e32 v37, v37, v18, vcc
	v_and_b32_e32 v38, 0x8000, v36
	v_cmp_gt_i32_e64 s[8:9], 0, v35
	v_cmp_gt_f32_e64 s[10:11], v19, v37
	v_cmp_eq_u32_e32 vcc, 0, v38
	s_or_b64 s[8:9], s[8:9], s[10:11]
	s_and_b64 vcc, vcc, s[8:9]
	v_cndmask_b32_e64 v35, v35, 15, vcc
	v_cndmask_b32_e32 v37, v37, v19, vcc
	v_and_b32_e32 v38, 0x10000, v36
	v_cmp_gt_i32_e64 s[8:9], 0, v35
	v_cmp_gt_f32_e64 s[10:11], v16, v37
	v_cmp_eq_u32_e32 vcc, 0, v38
	s_or_b64 s[8:9], s[8:9], s[10:11]
	s_and_b64 vcc, vcc, s[8:9]
	v_cndmask_b32_e64 v35, v35, 16, vcc
	v_cndmask_b32_e32 v37, v37, v16, vcc
	v_and_b32_e32 v38, 0x20000, v36
	v_cmp_gt_i32_e64 s[8:9], 0, v35
	v_cmp_gt_f32_e64 s[10:11], v17, v37
	v_cmp_eq_u32_e32 vcc, 0, v38
	s_or_b64 s[8:9], s[8:9], s[10:11]
	s_and_b64 vcc, vcc, s[8:9]
	v_cndmask_b32_e64 v35, v35, 17, vcc
	v_cndmask_b32_e32 v37, v37, v17, vcc
	v_and_b32_e32 v38, 0x40000, v36
	v_cmp_gt_i32_e64 s[8:9], 0, v35
	v_cmp_gt_f32_e64 s[10:11], v14, v37
	v_cmp_eq_u32_e32 vcc, 0, v38
	s_or_b64 s[8:9], s[8:9], s[10:11]
	s_and_b64 vcc, vcc, s[8:9]
	v_cndmask_b32_e64 v35, v35, 18, vcc
	v_cndmask_b32_e32 v37, v37, v14, vcc
	v_and_b32_e32 v38, 0x80000, v36
	v_cmp_gt_i32_e64 s[8:9], 0, v35
	v_cmp_gt_f32_e64 s[10:11], v15, v37
	v_cmp_eq_u32_e32 vcc, 0, v38
	s_or_b64 s[8:9], s[8:9], s[10:11]
	s_and_b64 vcc, vcc, s[8:9]
	v_cndmask_b32_e64 v35, v35, 19, vcc
	v_cndmask_b32_e32 v37, v37, v15, vcc
	v_and_b32_e32 v38, 0x100000, v36
	v_cmp_gt_i32_e64 s[8:9], 0, v35
	v_cmp_gt_f32_e64 s[10:11], v12, v37
	v_cmp_eq_u32_e32 vcc, 0, v38
	s_or_b64 s[8:9], s[8:9], s[10:11]
	s_and_b64 vcc, vcc, s[8:9]
	v_cndmask_b32_e64 v35, v35, 20, vcc
	v_cndmask_b32_e32 v37, v37, v12, vcc
	v_and_b32_e32 v38, 0x200000, v36
	v_cmp_gt_i32_e64 s[8:9], 0, v35
	v_cmp_gt_f32_e64 s[10:11], v13, v37
	v_cmp_eq_u32_e32 vcc, 0, v38
	s_or_b64 s[8:9], s[8:9], s[10:11]
	s_and_b64 vcc, vcc, s[8:9]
	v_cndmask_b32_e64 v35, v35, 21, vcc
	v_cndmask_b32_e32 v37, v37, v13, vcc
	v_and_b32_e32 v38, 0x400000, v36
	v_cmp_gt_i32_e64 s[8:9], 0, v35
	v_cmp_gt_f32_e64 s[10:11], v10, v37
	v_cmp_eq_u32_e32 vcc, 0, v38
	s_or_b64 s[8:9], s[8:9], s[10:11]
	s_and_b64 vcc, vcc, s[8:9]
	v_cndmask_b32_e64 v35, v35, 22, vcc
	v_cndmask_b32_e32 v37, v37, v10, vcc
	v_and_b32_e32 v38, 0x800000, v36
	v_cmp_gt_i32_e64 s[8:9], 0, v35
	v_cmp_gt_f32_e64 s[10:11], v11, v37
	v_cmp_eq_u32_e32 vcc, 0, v38
	s_or_b64 s[8:9], s[8:9], s[10:11]
	s_and_b64 vcc, vcc, s[8:9]
	v_cndmask_b32_e64 v35, v35, 23, vcc
	v_cndmask_b32_e32 v37, v37, v11, vcc
	v_and_b32_e32 v38, 0x1000000, v36
	v_cmp_gt_i32_e64 s[8:9], 0, v35
	v_cmp_gt_f32_e64 s[10:11], v8, v37
	v_cmp_eq_u32_e32 vcc, 0, v38
	s_or_b64 s[8:9], s[8:9], s[10:11]
	s_and_b64 vcc, vcc, s[8:9]
	v_cndmask_b32_e64 v35, v35, 24, vcc
	v_cndmask_b32_e32 v37, v37, v8, vcc
	v_and_b32_e32 v38, 0x2000000, v36
	v_cmp_gt_i32_e64 s[8:9], 0, v35
	v_cmp_gt_f32_e64 s[10:11], v9, v37
	v_cmp_eq_u32_e32 vcc, 0, v38
	s_or_b64 s[8:9], s[8:9], s[10:11]
	s_and_b64 vcc, vcc, s[8:9]
	v_cndmask_b32_e64 v35, v35, 25, vcc
	v_cndmask_b32_e32 v37, v37, v9, vcc
	v_and_b32_e32 v38, 0x4000000, v36
	v_cmp_gt_i32_e64 s[8:9], 0, v35
	v_cmp_gt_f32_e64 s[10:11], v6, v37
	v_cmp_eq_u32_e32 vcc, 0, v38
	s_or_b64 s[8:9], s[8:9], s[10:11]
	s_and_b64 vcc, vcc, s[8:9]
	v_cndmask_b32_e64 v35, v35, 26, vcc
	v_cndmask_b32_e32 v37, v37, v6, vcc
	v_and_b32_e32 v38, 0x8000000, v36
	v_cmp_gt_i32_e64 s[8:9], 0, v35
	v_cmp_gt_f32_e64 s[10:11], v7, v37
	v_cmp_eq_u32_e32 vcc, 0, v38
	s_or_b64 s[8:9], s[8:9], s[10:11]
	s_and_b64 vcc, vcc, s[8:9]
	v_cndmask_b32_e64 v35, v35, 27, vcc
	v_cndmask_b32_e32 v37, v37, v7, vcc
	v_and_b32_e32 v38, 0x10000000, v36
	v_cmp_gt_i32_e64 s[8:9], 0, v35
	v_cmp_gt_f32_e64 s[10:11], v4, v37
	v_cmp_eq_u32_e32 vcc, 0, v38
	s_or_b64 s[8:9], s[8:9], s[10:11]
	s_and_b64 vcc, vcc, s[8:9]
	v_cndmask_b32_e64 v35, v35, 28, vcc
	v_cndmask_b32_e32 v37, v37, v4, vcc
	v_and_b32_e32 v38, 0x20000000, v36
	v_cmp_gt_i32_e64 s[8:9], 0, v35
	v_cmp_gt_f32_e64 s[10:11], v5, v37
	v_cmp_eq_u32_e32 vcc, 0, v38
	s_or_b64 s[8:9], s[8:9], s[10:11]
	s_and_b64 vcc, vcc, s[8:9]
	v_cndmask_b32_e64 v35, v35, 29, vcc
	v_cndmask_b32_e32 v37, v37, v5, vcc
	v_and_b32_e32 v38, 2.0, v36
	v_cmp_gt_i32_e64 s[8:9], 0, v35
	v_cmp_gt_f32_e64 s[10:11], v2, v37
	v_cmp_eq_u32_e32 vcc, 0, v38
	s_or_b64 s[8:9], s[8:9], s[10:11]
	s_and_b64 vcc, vcc, s[8:9]
	v_cndmask_b32_e64 v35, v35, 30, vcc
	v_cndmask_b32_e32 v37, v37, v2, vcc
	v_cmp_gt_i32_e32 vcc, 0, v35
	v_cmp_gt_f32_e64 s[8:9], v3, v37
	s_or_b64 vcc, vcc, s[8:9]
	v_cndmask_b32_e64 v38, v35, 31, vcc
	v_cndmask_b32_e32 v39, v37, v3, vcc
	v_cmp_eq_u32_e32 vcc, 31, v146
	s_nop 1
	v_cndmask_b32_e32 v150, v38, v35, vcc
	v_lshl_or_b32 v36, 1, v150, v36
	v_cndmask_b32_e32 v35, v39, v37, vcc
	v_and_b32_e32 v37, 1, v36
	v_cmp_eq_u32_e32 vcc, 1, v37
	v_and_b32_e32 v39, 2, v36
	v_bfe_i32 v38, v36, 0, 1
	v_cndmask_b32_e32 v37, v32, v198, vcc
	v_cmp_gt_f32_e64 s[8:9], v33, v37
	s_or_b64 vcc, vcc, s[8:9]
	v_cndmask_b32_e64 v40, 0, 1, vcc
	v_cndmask_b32_e32 v41, v32, v33, vcc
	v_cmp_eq_u32_e32 vcc, 0, v39
	v_and_b32_e32 v39, 4, v36
	s_nop 0
	v_cndmask_b32_e32 v38, v38, v40, vcc
	v_cndmask_b32_e32 v37, v37, v41, vcc
	v_cmp_eq_u32_e32 vcc, 0, v39
	v_and_b32_e32 v39, 3, v36
	v_cmp_eq_u32_e64 s[8:9], 3, v39
	v_cmp_gt_f32_e64 s[10:11], v30, v37
	s_or_b64 s[8:9], s[8:9], s[10:11]
	s_and_b64 vcc, vcc, s[8:9]
	v_cndmask_b32_e64 v38, v38, 2, vcc
	v_cndmask_b32_e32 v37, v37, v30, vcc
	v_and_b32_e32 v39, 8, v36
	v_cmp_gt_i32_e64 s[8:9], 0, v38
	v_cmp_gt_f32_e64 s[10:11], v31, v37
	v_cmp_eq_u32_e32 vcc, 0, v39
	s_or_b64 s[8:9], s[8:9], s[10:11]
	s_and_b64 vcc, vcc, s[8:9]
	v_cndmask_b32_e64 v38, v38, 3, vcc
	v_cndmask_b32_e32 v37, v37, v31, vcc
	v_and_b32_e32 v39, 16, v36
	v_cmp_gt_i32_e64 s[8:9], 0, v38
	v_cmp_gt_f32_e64 s[10:11], v28, v37
	v_cmp_eq_u32_e32 vcc, 0, v39
	s_or_b64 s[8:9], s[8:9], s[10:11]
	s_and_b64 vcc, vcc, s[8:9]
	v_cndmask_b32_e64 v38, v38, 4, vcc
	v_cndmask_b32_e32 v37, v37, v28, vcc
	v_and_b32_e32 v39, 32, v36
	v_cmp_gt_i32_e64 s[8:9], 0, v38
	v_cmp_gt_f32_e64 s[10:11], v29, v37
	v_cmp_eq_u32_e32 vcc, 0, v39
	s_or_b64 s[8:9], s[8:9], s[10:11]
	s_and_b64 vcc, vcc, s[8:9]
	v_cndmask_b32_e64 v38, v38, 5, vcc
	v_cndmask_b32_e32 v37, v37, v29, vcc
	v_and_b32_e32 v39, 64, v36
	v_cmp_gt_i32_e64 s[8:9], 0, v38
	v_cmp_gt_f32_e64 s[10:11], v26, v37
	v_cmp_eq_u32_e32 vcc, 0, v39
	s_or_b64 s[8:9], s[8:9], s[10:11]
	s_and_b64 vcc, vcc, s[8:9]
	v_cndmask_b32_e64 v38, v38, 6, vcc
	v_cndmask_b32_e32 v37, v37, v26, vcc
	v_and_b32_e32 v39, 0x80, v36
	v_cmp_gt_i32_e64 s[8:9], 0, v38
	v_cmp_gt_f32_e64 s[10:11], v27, v37
	v_cmp_eq_u32_e32 vcc, 0, v39
	s_or_b64 s[8:9], s[8:9], s[10:11]
	s_and_b64 vcc, vcc, s[8:9]
	v_cndmask_b32_e64 v38, v38, 7, vcc
	v_cndmask_b32_e32 v37, v37, v27, vcc
	v_and_b32_e32 v39, 0x100, v36
	v_cmp_gt_i32_e64 s[8:9], 0, v38
	v_cmp_gt_f32_e64 s[10:11], v24, v37
	v_cmp_eq_u32_e32 vcc, 0, v39
	s_or_b64 s[8:9], s[8:9], s[10:11]
	s_and_b64 vcc, vcc, s[8:9]
	v_cndmask_b32_e64 v38, v38, 8, vcc
	v_cndmask_b32_e32 v37, v37, v24, vcc
	v_and_b32_e32 v39, 0x200, v36
	v_cmp_gt_i32_e64 s[8:9], 0, v38
	v_cmp_gt_f32_e64 s[10:11], v25, v37
	v_cmp_eq_u32_e32 vcc, 0, v39
	s_or_b64 s[8:9], s[8:9], s[10:11]
	s_and_b64 vcc, vcc, s[8:9]
	v_cndmask_b32_e64 v38, v38, 9, vcc
	v_cndmask_b32_e32 v37, v37, v25, vcc
	v_and_b32_e32 v39, 0x400, v36
	v_cmp_gt_i32_e64 s[8:9], 0, v38
	v_cmp_gt_f32_e64 s[10:11], v22, v37
	v_cmp_eq_u32_e32 vcc, 0, v39
	s_or_b64 s[8:9], s[8:9], s[10:11]
	s_and_b64 vcc, vcc, s[8:9]
	v_cndmask_b32_e64 v38, v38, 10, vcc
	v_cndmask_b32_e32 v37, v37, v22, vcc
	v_and_b32_e32 v39, 0x800, v36
	v_cmp_gt_i32_e64 s[8:9], 0, v38
	v_cmp_gt_f32_e64 s[10:11], v23, v37
	v_cmp_eq_u32_e32 vcc, 0, v39
	s_or_b64 s[8:9], s[8:9], s[10:11]
	s_and_b64 vcc, vcc, s[8:9]
	v_cndmask_b32_e64 v38, v38, 11, vcc
	v_cndmask_b32_e32 v37, v37, v23, vcc
	v_and_b32_e32 v39, 0x1000, v36
	v_cmp_gt_i32_e64 s[8:9], 0, v38
	v_cmp_gt_f32_e64 s[10:11], v20, v37
	v_cmp_eq_u32_e32 vcc, 0, v39
	s_or_b64 s[8:9], s[8:9], s[10:11]
	s_and_b64 vcc, vcc, s[8:9]
	v_cndmask_b32_e64 v38, v38, 12, vcc
	v_cndmask_b32_e32 v37, v37, v20, vcc
	v_and_b32_e32 v39, 0x2000, v36
	v_cmp_gt_i32_e64 s[8:9], 0, v38
	v_cmp_gt_f32_e64 s[10:11], v21, v37
	v_cmp_eq_u32_e32 vcc, 0, v39
	s_or_b64 s[8:9], s[8:9], s[10:11]
	s_and_b64 vcc, vcc, s[8:9]
	v_cndmask_b32_e64 v38, v38, 13, vcc
	v_cndmask_b32_e32 v37, v37, v21, vcc
	v_and_b32_e32 v39, 0x4000, v36
	v_cmp_gt_i32_e64 s[8:9], 0, v38
	v_cmp_gt_f32_e64 s[10:11], v18, v37
	v_cmp_eq_u32_e32 vcc, 0, v39
	s_or_b64 s[8:9], s[8:9], s[10:11]
	s_and_b64 vcc, vcc, s[8:9]
	v_cndmask_b32_e64 v38, v38, 14, vcc
	v_cndmask_b32_e32 v37, v37, v18, vcc
	v_and_b32_e32 v39, 0x8000, v36
	v_cmp_gt_i32_e64 s[8:9], 0, v38
	v_cmp_gt_f32_e64 s[10:11], v19, v37
	v_cmp_eq_u32_e32 vcc, 0, v39
	s_or_b64 s[8:9], s[8:9], s[10:11]
	s_and_b64 vcc, vcc, s[8:9]
	v_cndmask_b32_e64 v38, v38, 15, vcc
	v_cndmask_b32_e32 v37, v37, v19, vcc
	v_and_b32_e32 v39, 0x10000, v36
	v_cmp_gt_i32_e64 s[8:9], 0, v38
	v_cmp_gt_f32_e64 s[10:11], v16, v37
	v_cmp_eq_u32_e32 vcc, 0, v39
	s_or_b64 s[8:9], s[8:9], s[10:11]
	s_and_b64 vcc, vcc, s[8:9]
	v_cndmask_b32_e64 v38, v38, 16, vcc
	v_cndmask_b32_e32 v37, v37, v16, vcc
	v_and_b32_e32 v39, 0x20000, v36
	v_cmp_gt_i32_e64 s[8:9], 0, v38
	v_cmp_gt_f32_e64 s[10:11], v17, v37
	v_cmp_eq_u32_e32 vcc, 0, v39
	s_or_b64 s[8:9], s[8:9], s[10:11]
	s_and_b64 vcc, vcc, s[8:9]
	v_cndmask_b32_e64 v38, v38, 17, vcc
	v_cndmask_b32_e32 v37, v37, v17, vcc
	v_and_b32_e32 v39, 0x40000, v36
	v_cmp_gt_i32_e64 s[8:9], 0, v38
	v_cmp_gt_f32_e64 s[10:11], v14, v37
	v_cmp_eq_u32_e32 vcc, 0, v39
	s_or_b64 s[8:9], s[8:9], s[10:11]
	s_and_b64 vcc, vcc, s[8:9]
	v_cndmask_b32_e64 v38, v38, 18, vcc
	v_cndmask_b32_e32 v37, v37, v14, vcc
	v_and_b32_e32 v39, 0x80000, v36
	v_cmp_gt_i32_e64 s[8:9], 0, v38
	v_cmp_gt_f32_e64 s[10:11], v15, v37
	v_cmp_eq_u32_e32 vcc, 0, v39
	s_or_b64 s[8:9], s[8:9], s[10:11]
	s_and_b64 vcc, vcc, s[8:9]
	v_cndmask_b32_e64 v38, v38, 19, vcc
	v_cndmask_b32_e32 v37, v37, v15, vcc
	v_and_b32_e32 v39, 0x100000, v36
	v_cmp_gt_i32_e64 s[8:9], 0, v38
	v_cmp_gt_f32_e64 s[10:11], v12, v37
	v_cmp_eq_u32_e32 vcc, 0, v39
	s_or_b64 s[8:9], s[8:9], s[10:11]
	s_and_b64 vcc, vcc, s[8:9]
	v_cndmask_b32_e64 v38, v38, 20, vcc
	v_cndmask_b32_e32 v37, v37, v12, vcc
	v_and_b32_e32 v39, 0x200000, v36
	v_cmp_gt_i32_e64 s[8:9], 0, v38
	v_cmp_gt_f32_e64 s[10:11], v13, v37
	v_cmp_eq_u32_e32 vcc, 0, v39
	s_or_b64 s[8:9], s[8:9], s[10:11]
	s_and_b64 vcc, vcc, s[8:9]
	v_cndmask_b32_e64 v38, v38, 21, vcc
	v_cndmask_b32_e32 v37, v37, v13, vcc
	v_and_b32_e32 v39, 0x400000, v36
	v_cmp_gt_i32_e64 s[8:9], 0, v38
	v_cmp_gt_f32_e64 s[10:11], v10, v37
	v_cmp_eq_u32_e32 vcc, 0, v39
	s_or_b64 s[8:9], s[8:9], s[10:11]
	s_and_b64 vcc, vcc, s[8:9]
	v_cndmask_b32_e64 v38, v38, 22, vcc
	v_cndmask_b32_e32 v37, v37, v10, vcc
	v_and_b32_e32 v39, 0x800000, v36
	v_cmp_gt_i32_e64 s[8:9], 0, v38
	v_cmp_gt_f32_e64 s[10:11], v11, v37
	v_cmp_eq_u32_e32 vcc, 0, v39
	s_or_b64 s[8:9], s[8:9], s[10:11]
	s_and_b64 vcc, vcc, s[8:9]
	v_cndmask_b32_e64 v38, v38, 23, vcc
	v_cndmask_b32_e32 v37, v37, v11, vcc
	v_and_b32_e32 v39, 0x1000000, v36
	v_cmp_gt_i32_e64 s[8:9], 0, v38
	v_cmp_gt_f32_e64 s[10:11], v8, v37
	v_cmp_eq_u32_e32 vcc, 0, v39
	s_or_b64 s[8:9], s[8:9], s[10:11]
	s_and_b64 vcc, vcc, s[8:9]
	v_cndmask_b32_e64 v38, v38, 24, vcc
	v_cndmask_b32_e32 v37, v37, v8, vcc
	v_and_b32_e32 v39, 0x2000000, v36
	v_cmp_gt_i32_e64 s[8:9], 0, v38
	v_cmp_gt_f32_e64 s[10:11], v9, v37
	v_cmp_eq_u32_e32 vcc, 0, v39
	s_or_b64 s[8:9], s[8:9], s[10:11]
	s_and_b64 vcc, vcc, s[8:9]
	v_cndmask_b32_e64 v38, v38, 25, vcc
	v_cndmask_b32_e32 v37, v37, v9, vcc
	v_and_b32_e32 v39, 0x4000000, v36
	v_cmp_gt_i32_e64 s[8:9], 0, v38
	v_cmp_gt_f32_e64 s[10:11], v6, v37
	v_cmp_eq_u32_e32 vcc, 0, v39
	s_or_b64 s[8:9], s[8:9], s[10:11]
	s_and_b64 vcc, vcc, s[8:9]
	v_cndmask_b32_e64 v38, v38, 26, vcc
	v_cndmask_b32_e32 v37, v37, v6, vcc
	v_and_b32_e32 v39, 0x8000000, v36
	v_cmp_gt_i32_e64 s[8:9], 0, v38
	v_cmp_gt_f32_e64 s[10:11], v7, v37
	v_cmp_eq_u32_e32 vcc, 0, v39
	s_or_b64 s[8:9], s[8:9], s[10:11]
	s_and_b64 vcc, vcc, s[8:9]
	v_cndmask_b32_e64 v38, v38, 27, vcc
	v_cndmask_b32_e32 v37, v37, v7, vcc
	v_and_b32_e32 v39, 0x10000000, v36
	v_cmp_gt_i32_e64 s[8:9], 0, v38
	v_cmp_gt_f32_e64 s[10:11], v4, v37
	v_cmp_eq_u32_e32 vcc, 0, v39
	s_or_b64 s[8:9], s[8:9], s[10:11]
	s_and_b64 vcc, vcc, s[8:9]
	v_cndmask_b32_e64 v38, v38, 28, vcc
	v_cndmask_b32_e32 v37, v37, v4, vcc
	v_and_b32_e32 v39, 0x20000000, v36
	v_cmp_gt_i32_e64 s[8:9], 0, v38
	v_cmp_gt_f32_e64 s[10:11], v5, v37
	v_cmp_eq_u32_e32 vcc, 0, v39
	s_or_b64 s[8:9], s[8:9], s[10:11]
	s_and_b64 vcc, vcc, s[8:9]
	v_cndmask_b32_e64 v38, v38, 29, vcc
	v_cndmask_b32_e32 v37, v37, v5, vcc
	v_and_b32_e32 v39, 2.0, v36
	v_cmp_gt_i32_e64 s[8:9], 0, v38
	v_cmp_gt_f32_e64 s[10:11], v2, v37
	v_cmp_eq_u32_e32 vcc, 0, v39
	s_or_b64 s[8:9], s[8:9], s[10:11]
	s_and_b64 vcc, vcc, s[8:9]
	v_cndmask_b32_e64 v38, v38, 30, vcc
	v_cndmask_b32_e32 v37, v37, v2, vcc
	v_cmp_gt_i32_e64 s[8:9], 0, v38
	v_cmp_gt_f32_e64 s[10:11], v3, v37
	v_cmp_lt_i32_e32 vcc, -1, v36
	s_or_b64 s[8:9], s[8:9], s[10:11]
	s_and_b64 vcc, vcc, s[8:9]
	v_cndmask_b32_e64 v154, v38, 31, vcc
	v_lshlrev_b32_e64 v38, v154, 1
	v_or_b32_e32 v39, v38, v36
	v_and_b32_e32 v40, 1, v39
	v_cndmask_b32_e32 v37, v37, v3, vcc
	v_cmp_eq_u32_e32 vcc, 1, v40
	v_bitop3_b32 v42, v38, 2, v36 bitop3:0xc8
	v_bfe_i32 v41, v39, 0, 1
	v_cndmask_b32_e32 v40, v32, v198, vcc
	v_cmp_gt_f32_e64 s[8:9], v33, v40
	s_or_b64 vcc, vcc, s[8:9]
	v_cndmask_b32_e64 v43, 0, 1, vcc
	v_cndmask_b32_e32 v32, v32, v33, vcc
	v_cmp_eq_u32_e32 vcc, 0, v42
	s_nop 1
	v_cndmask_b32_e32 v32, v40, v32, vcc
	v_bitop3_b32 v40, v38, 4, v36 bitop3:0xc8
	v_cndmask_b32_e32 v33, v41, v43, vcc
	v_cmp_eq_u32_e32 vcc, 0, v40
	v_bitop3_b32 v40, v38, 3, v36 bitop3:0xc8
	v_cmp_eq_u32_e64 s[8:9], 3, v40
	v_cmp_gt_f32_e64 s[10:11], v30, v32
	s_or_b64 s[8:9], s[8:9], s[10:11]
	s_and_b64 vcc, vcc, s[8:9]
	v_cndmask_b32_e64 v33, v33, 2, vcc
	v_cndmask_b32_e32 v30, v32, v30, vcc
	v_bitop3_b32 v32, v38, 8, v36 bitop3:0xc8
	v_cmp_gt_i32_e64 s[8:9], 0, v33
	v_cmp_gt_f32_e64 s[10:11], v31, v30
	v_cmp_eq_u32_e32 vcc, 0, v32
	s_or_b64 s[8:9], s[8:9], s[10:11]
	s_and_b64 vcc, vcc, s[8:9]
	v_cndmask_b32_e64 v32, v33, 3, vcc
	v_cndmask_b32_e32 v30, v30, v31, vcc
	v_bitop3_b32 v31, v38, 16, v36 bitop3:0xc8
	v_cmp_gt_i32_e64 s[8:9], 0, v32
	v_cmp_gt_f32_e64 s[10:11], v28, v30
	v_cmp_eq_u32_e32 vcc, 0, v31
	s_or_b64 s[8:9], s[8:9], s[10:11]
	s_and_b64 vcc, vcc, s[8:9]
	v_cndmask_b32_e64 v31, v32, 4, vcc
	v_cndmask_b32_e32 v28, v30, v28, vcc
	v_bitop3_b32 v30, v38, 32, v36 bitop3:0xc8
	v_cmp_gt_i32_e64 s[8:9], 0, v31
	v_cmp_gt_f32_e64 s[10:11], v29, v28
	v_cmp_eq_u32_e32 vcc, 0, v30
	s_or_b64 s[8:9], s[8:9], s[10:11]
	s_and_b64 vcc, vcc, s[8:9]
	v_cndmask_b32_e64 v30, v31, 5, vcc
	v_cndmask_b32_e32 v28, v28, v29, vcc
	v_bitop3_b32 v29, v38, 64, v36 bitop3:0xc8
	v_cmp_gt_i32_e64 s[8:9], 0, v30
	v_cmp_gt_f32_e64 s[10:11], v26, v28
	v_cmp_eq_u32_e32 vcc, 0, v29
	s_or_b64 s[8:9], s[8:9], s[10:11]
	s_and_b64 vcc, vcc, s[8:9]
	v_cndmask_b32_e64 v29, v30, 6, vcc
	v_cndmask_b32_e32 v26, v28, v26, vcc
	v_bitop3_b32 v28, v38, s26, v36 bitop3:0xc8
	v_cmp_gt_i32_e64 s[8:9], 0, v29
	v_cmp_gt_f32_e64 s[10:11], v27, v26
	v_cmp_eq_u32_e32 vcc, 0, v28
	s_or_b64 s[8:9], s[8:9], s[10:11]
	s_and_b64 vcc, vcc, s[8:9]
	v_cndmask_b32_e64 v28, v29, 7, vcc
	v_cndmask_b32_e32 v26, v26, v27, vcc
	v_bitop3_b32 v27, v38, s27, v36 bitop3:0xc8
	v_cmp_gt_i32_e64 s[8:9], 0, v28
	v_cmp_gt_f32_e64 s[10:11], v24, v26
	v_cmp_eq_u32_e32 vcc, 0, v27
	s_or_b64 s[8:9], s[8:9], s[10:11]
	s_and_b64 vcc, vcc, s[8:9]
	v_cndmask_b32_e64 v27, v28, 8, vcc
	v_cndmask_b32_e32 v24, v26, v24, vcc
	v_bitop3_b32 v26, v38, s28, v36 bitop3:0xc8
	v_cmp_gt_i32_e64 s[8:9], 0, v27
	v_cmp_gt_f32_e64 s[10:11], v25, v24
	v_cmp_eq_u32_e32 vcc, 0, v26
	s_or_b64 s[8:9], s[8:9], s[10:11]
	s_and_b64 vcc, vcc, s[8:9]
	v_cndmask_b32_e64 v26, v27, 9, vcc
	v_cndmask_b32_e32 v24, v24, v25, vcc
	v_bitop3_b32 v25, v38, s29, v36 bitop3:0xc8
	v_cmp_gt_i32_e64 s[8:9], 0, v26
	v_cmp_gt_f32_e64 s[10:11], v22, v24
	v_cmp_eq_u32_e32 vcc, 0, v25
	s_or_b64 s[8:9], s[8:9], s[10:11]
	s_and_b64 vcc, vcc, s[8:9]
	v_cndmask_b32_e64 v25, v26, 10, vcc
	v_cndmask_b32_e32 v22, v24, v22, vcc
	v_bitop3_b32 v24, v38, s30, v36 bitop3:0xc8
	v_cmp_gt_i32_e64 s[8:9], 0, v25
	v_cmp_gt_f32_e64 s[10:11], v23, v22
	v_cmp_eq_u32_e32 vcc, 0, v24
	s_or_b64 s[8:9], s[8:9], s[10:11]
	s_and_b64 vcc, vcc, s[8:9]
	v_cndmask_b32_e64 v24, v25, 11, vcc
	v_cndmask_b32_e32 v22, v22, v23, vcc
	v_bitop3_b32 v23, v38, s31, v36 bitop3:0xc8
	v_cmp_gt_i32_e64 s[8:9], 0, v24
	v_cmp_gt_f32_e64 s[10:11], v20, v22
	v_cmp_eq_u32_e32 vcc, 0, v23
	s_or_b64 s[8:9], s[8:9], s[10:11]
	s_and_b64 vcc, vcc, s[8:9]
	v_cndmask_b32_e64 v23, v24, 12, vcc
	v_cndmask_b32_e32 v20, v22, v20, vcc
	v_bitop3_b32 v22, v38, s33, v36 bitop3:0xc8
	v_cmp_gt_i32_e64 s[8:9], 0, v23
	v_cmp_gt_f32_e64 s[10:11], v21, v20
	v_cmp_eq_u32_e32 vcc, 0, v22
	s_or_b64 s[8:9], s[8:9], s[10:11]
	s_and_b64 vcc, vcc, s[8:9]
	v_cndmask_b32_e64 v22, v23, 13, vcc
	v_cndmask_b32_e32 v20, v20, v21, vcc
	v_bitop3_b32 v21, v38, s34, v36 bitop3:0xc8
	v_cmp_gt_i32_e64 s[8:9], 0, v22
	v_cmp_gt_f32_e64 s[10:11], v18, v20
	v_cmp_eq_u32_e32 vcc, 0, v21
	s_or_b64 s[8:9], s[8:9], s[10:11]
	s_and_b64 vcc, vcc, s[8:9]
	v_cndmask_b32_e64 v21, v22, 14, vcc
	v_cndmask_b32_e32 v18, v20, v18, vcc
	v_bitop3_b32 v20, v38, s35, v36 bitop3:0xc8
	v_cmp_gt_i32_e64 s[8:9], 0, v21
	v_cmp_gt_f32_e64 s[10:11], v19, v18
	v_cmp_eq_u32_e32 vcc, 0, v20
	s_or_b64 s[8:9], s[8:9], s[10:11]
	s_and_b64 vcc, vcc, s[8:9]
	v_cndmask_b32_e64 v20, v21, 15, vcc
	v_cndmask_b32_e32 v18, v18, v19, vcc
	v_bitop3_b32 v19, v38, s36, v36 bitop3:0xc8
	v_cmp_gt_i32_e64 s[8:9], 0, v20
	v_cmp_gt_f32_e64 s[10:11], v16, v18
	v_cmp_eq_u32_e32 vcc, 0, v19
	s_or_b64 s[8:9], s[8:9], s[10:11]
	s_and_b64 vcc, vcc, s[8:9]
	v_cndmask_b32_e64 v19, v20, 16, vcc
	v_cndmask_b32_e32 v16, v18, v16, vcc
	v_bitop3_b32 v18, v38, s37, v36 bitop3:0xc8
	v_cmp_gt_i32_e64 s[8:9], 0, v19
	v_cmp_gt_f32_e64 s[10:11], v17, v16
	v_cmp_eq_u32_e32 vcc, 0, v18
	s_or_b64 s[8:9], s[8:9], s[10:11]
	s_and_b64 vcc, vcc, s[8:9]
	v_cndmask_b32_e64 v18, v19, 17, vcc
	v_cndmask_b32_e32 v16, v16, v17, vcc
	v_bitop3_b32 v17, v38, s38, v36 bitop3:0xc8
	v_cmp_gt_i32_e64 s[8:9], 0, v18
	v_cmp_gt_f32_e64 s[10:11], v14, v16
	v_cmp_eq_u32_e32 vcc, 0, v17
	s_or_b64 s[8:9], s[8:9], s[10:11]
	s_and_b64 vcc, vcc, s[8:9]
	v_cndmask_b32_e64 v17, v18, 18, vcc
	v_cndmask_b32_e32 v14, v16, v14, vcc
	v_bitop3_b32 v16, v38, s39, v36 bitop3:0xc8
	v_cmp_gt_i32_e64 s[8:9], 0, v17
	v_cmp_gt_f32_e64 s[10:11], v15, v14
	v_cmp_eq_u32_e32 vcc, 0, v16
	s_or_b64 s[8:9], s[8:9], s[10:11]
	s_and_b64 vcc, vcc, s[8:9]
	v_cndmask_b32_e64 v16, v17, 19, vcc
	v_cndmask_b32_e32 v14, v14, v15, vcc
	v_bitop3_b32 v15, v38, s40, v36 bitop3:0xc8
	v_cmp_gt_i32_e64 s[8:9], 0, v16
	v_cmp_gt_f32_e64 s[10:11], v12, v14
	v_cmp_eq_u32_e32 vcc, 0, v15
	s_or_b64 s[8:9], s[8:9], s[10:11]
	s_and_b64 vcc, vcc, s[8:9]
	v_cndmask_b32_e64 v15, v16, 20, vcc
	v_cndmask_b32_e32 v12, v14, v12, vcc
	v_bitop3_b32 v14, v38, s41, v36 bitop3:0xc8
	v_cmp_gt_i32_e64 s[8:9], 0, v15
	v_cmp_gt_f32_e64 s[10:11], v13, v12
	v_cmp_eq_u32_e32 vcc, 0, v14
	s_or_b64 s[8:9], s[8:9], s[10:11]
	s_and_b64 vcc, vcc, s[8:9]
	v_cndmask_b32_e64 v14, v15, 21, vcc
	v_cndmask_b32_e32 v12, v12, v13, vcc
	v_bitop3_b32 v13, v38, s42, v36 bitop3:0xc8
	v_cmp_gt_i32_e64 s[8:9], 0, v14
	v_cmp_gt_f32_e64 s[10:11], v10, v12
	v_cmp_eq_u32_e32 vcc, 0, v13
	s_or_b64 s[8:9], s[8:9], s[10:11]
	s_and_b64 vcc, vcc, s[8:9]
	v_cndmask_b32_e64 v13, v14, 22, vcc
	v_cndmask_b32_e32 v10, v12, v10, vcc
	v_bitop3_b32 v12, v38, s43, v36 bitop3:0xc8
	v_cmp_gt_i32_e64 s[8:9], 0, v13
	v_cmp_gt_f32_e64 s[10:11], v11, v10
	v_cmp_eq_u32_e32 vcc, 0, v12
	s_or_b64 s[8:9], s[8:9], s[10:11]
	s_and_b64 vcc, vcc, s[8:9]
	v_cndmask_b32_e64 v12, v13, 23, vcc
	v_cndmask_b32_e32 v10, v10, v11, vcc
	v_bitop3_b32 v11, v38, s44, v36 bitop3:0xc8
	v_cmp_gt_i32_e64 s[8:9], 0, v12
	v_cmp_gt_f32_e64 s[10:11], v8, v10
	v_cmp_eq_u32_e32 vcc, 0, v11
	s_or_b64 s[8:9], s[8:9], s[10:11]
	s_and_b64 vcc, vcc, s[8:9]
	v_cndmask_b32_e64 v11, v12, 24, vcc
	v_cndmask_b32_e32 v8, v10, v8, vcc
	v_bitop3_b32 v10, v38, s45, v36 bitop3:0xc8
	v_cmp_gt_i32_e64 s[8:9], 0, v11
	v_cmp_gt_f32_e64 s[10:11], v9, v8
	v_cmp_eq_u32_e32 vcc, 0, v10
	s_or_b64 s[8:9], s[8:9], s[10:11]
	s_and_b64 vcc, vcc, s[8:9]
	v_cndmask_b32_e64 v10, v11, 25, vcc
	v_cndmask_b32_e32 v8, v8, v9, vcc
	v_bitop3_b32 v9, v38, s46, v36 bitop3:0xc8
	v_cmp_gt_i32_e64 s[8:9], 0, v10
	v_cmp_gt_f32_e64 s[10:11], v6, v8
	v_cmp_eq_u32_e32 vcc, 0, v9
	s_or_b64 s[8:9], s[8:9], s[10:11]
	s_and_b64 vcc, vcc, s[8:9]
	v_cndmask_b32_e64 v9, v10, 26, vcc
	v_cndmask_b32_e32 v6, v8, v6, vcc
	v_bitop3_b32 v8, v38, s47, v36 bitop3:0xc8
	v_cmp_gt_i32_e64 s[8:9], 0, v9
	v_cmp_gt_f32_e64 s[10:11], v7, v6
	v_cmp_eq_u32_e32 vcc, 0, v8
	s_or_b64 s[8:9], s[8:9], s[10:11]
	s_and_b64 vcc, vcc, s[8:9]
	v_cndmask_b32_e64 v8, v9, 27, vcc
	v_cndmask_b32_e32 v6, v6, v7, vcc
	v_bitop3_b32 v7, v38, s48, v36 bitop3:0xc8
	v_cmp_gt_i32_e64 s[8:9], 0, v8
	v_cmp_gt_f32_e64 s[10:11], v4, v6
	v_cmp_eq_u32_e32 vcc, 0, v7
	s_or_b64 s[8:9], s[8:9], s[10:11]
	s_and_b64 vcc, vcc, s[8:9]
	v_cndmask_b32_e64 v7, v8, 28, vcc
	v_cndmask_b32_e32 v4, v6, v4, vcc
	v_bitop3_b32 v6, v38, s49, v36 bitop3:0xc8
	v_cmp_gt_i32_e64 s[8:9], 0, v7
	v_cmp_gt_f32_e64 s[10:11], v5, v4
	v_cmp_eq_u32_e32 vcc, 0, v6
	s_or_b64 s[8:9], s[8:9], s[10:11]
	s_and_b64 vcc, vcc, s[8:9]
	v_cndmask_b32_e64 v6, v7, 29, vcc
	v_cndmask_b32_e32 v4, v4, v5, vcc
	v_bitop3_b32 v5, v38, 2.0, v36 bitop3:0xc8
	v_cmp_gt_i32_e64 s[8:9], 0, v6
	v_cmp_gt_f32_e64 s[10:11], v2, v4
	v_cmp_eq_u32_e32 vcc, 0, v5
	s_or_b64 s[8:9], s[8:9], s[10:11]
	s_and_b64 vcc, vcc, s[8:9]
	v_cndmask_b32_e32 v2, v4, v2, vcc
	v_sub_f32_e32 v4, v35, v34
	v_cndmask_b32_e64 v5, v6, 30, vcc
	v_mul_f32_e32 v6, 0x3fb8aa3b, v4
	v_fma_f32 v7, v4, s50, -v6
	v_rndne_f32_e32 v8, v6
	v_fmac_f32_e32 v7, 0x32a5705f, v4
	v_sub_f32_e32 v6, v6, v8
	v_add_f32_e32 v6, v6, v7
	v_cmp_gt_i32_e64 s[8:9], 0, v5
	v_cmp_gt_f32_e64 s[10:11], v3, v2
	v_exp_f32_e32 v6, v6
	v_cvt_i32_f32_e32 v7, v8
	v_cmp_lt_i32_e32 vcc, -1, v39
	s_or_b64 s[8:9], s[8:9], s[10:11]
	s_and_b64 vcc, vcc, s[8:9]
	v_cndmask_b32_e64 v158, v5, 31, vcc
	v_sub_f32_e32 v5, v37, v34
	v_cndmask_b32_e32 v2, v2, v3, vcc
	v_ldexp_f32 v3, v6, v7
	v_mul_f32_e32 v6, 0x3fb8aa3b, v5
	v_fma_f32 v7, v5, s50, -v6
	v_rndne_f32_e32 v8, v6
	v_fmac_f32_e32 v7, 0x32a5705f, v5
	v_sub_f32_e32 v6, v6, v8
	v_add_f32_e32 v6, v6, v7
	v_exp_f32_e32 v6, v6
	v_cvt_i32_f32_e32 v7, v8
	v_cmp_ngt_f32_e32 vcc, s51, v4
	v_sub_f32_e32 v2, v2, v34
	s_nop 0
	v_cndmask_b32_e32 v3, 0, v3, vcc
	v_cmp_nlt_f32_e32 vcc, s52, v4
	s_nop 1
	v_cndmask_b32_e32 v4, v199, v3, vcc
	v_ldexp_f32 v3, v6, v7
	v_mul_f32_e32 v6, 0x3fb8aa3b, v2
	v_fma_f32 v7, v2, s50, -v6
	v_rndne_f32_e32 v8, v6
	v_fmac_f32_e32 v7, 0x32a5705f, v2
	v_sub_f32_e32 v6, v6, v8
	v_add_f32_e32 v6, v6, v7
	v_exp_f32_e32 v6, v6
	v_cvt_i32_f32_e32 v7, v8
	v_cmp_ngt_f32_e32 vcc, s51, v5
	s_nop 1
	v_cndmask_b32_e32 v3, 0, v3, vcc
	v_cmp_nlt_f32_e32 vcc, s52, v5
	v_ldexp_f32 v5, v6, v7
	s_nop 0
	v_cndmask_b32_e32 v3, v199, v3, vcc
	v_cmp_ngt_f32_e32 vcc, s51, v2
	s_nop 1
	v_cndmask_b32_e32 v5, 0, v5, vcc
	v_cmp_nlt_f32_e32 vcc, s52, v2
	s_nop 1
	v_cndmask_b32_e32 v2, v199, v5, vcc
	v_add_f32_e32 v5, 1.0, v4
	v_add_f32_e32 v5, v5, v3
	v_add_f32_e32 v5, v5, v2
	v_div_scale_f32 v6, s[8:9], v5, v5, 1.0
	v_rcp_f32_e32 v7, v6
	s_nop 0
	v_fma_f32 v8, -v6, v7, 1.0
	v_fmac_f32_e32 v7, v8, v7
	v_div_scale_f32 v8, vcc, 1.0, v5, 1.0
	v_mul_f32_e32 v9, v8, v7
	v_fma_f32 v10, -v6, v9, v8
	v_fmac_f32_e32 v9, v10, v7
	v_fma_f32 v6, -v6, v9, v8
	v_lshl_add_u32 v8, v146, 2, s1
	ds_add_rtn_u32 v205, v8, v197
	v_lshl_add_u32 v8, v150, 2, s1
	ds_add_rtn_u32 v207, v8, v197
	v_lshl_add_u32 v8, v154, 2, s1
	ds_add_rtn_u32 v208, v8, v197
	v_lshl_add_u32 v8, v158, 2, s1
	ds_add_rtn_u32 v209, v8, v197
	v_div_fmas_f32 v6, v6, v7, v9
	v_div_fixup_f32 v160, v6, v5, 1.0
	v_mul_f32_e32 v206, v4, v160
	v_pk_mul_f32 v[164:165], v[2:3], v[160:161] op_sel_hi:[1,0]
